# attention MFMA segments: LDS-read wait batching look-ahead 4 instead of 3 (counted-wait placement tuning)
# baseline (speedup 1.0000x reference)
.LBB0_528:
	ds_read_b128 v[88:91], v129
	ds_read_b128 v[92:95], v129 offset:1024
	ds_read_b128 v[96:99], v130
	ds_read_b128 v[152:155], v130 offset:1024
	ds_read_b128 v[176:179], v131
	ds_read_b128 v[180:183], v131 offset:1024
	ds_read_b128 v[184:187], v132
	ds_read_b128 v[188:191], v132 offset:1024
	ds_read_b128 v[192:195], v129 offset:8192
	ds_read_b128 v[196:199], v129 offset:9216
	ds_read_b128 v[200:203], v130 offset:8192
	ds_read_b128 v[204:207], v130 offset:9216
	ds_read_b128 v[208:211], v131 offset:8192
	ds_read_b128 v[212:215], v131 offset:9216
	ds_read_b128 v[216:219], v132 offset:8192
	s_and_b64 vcc, exec, s[10:11]
	s_waitcnt lgkmcnt(10)
	v_mfma_f32_16x16x32_bf16 v[72:75], v[88:91], v[0:3], v[240:243]
	ds_read_b128 v[220:223], v132 offset:9216
	ds_read_b64_tr_b16 v[224:225], v142 offset:49152
	ds_read_b64_tr_b16 v[226:227], v146 offset:49152
	ds_read_b64_tr_b16 v[230:231], v146 offset:57344
	ds_read_b64_tr_b16 v[228:229], v142 offset:57344
	v_mfma_f32_16x16x32_bf16 v[72:75], v[96:99], v[4:7], v[72:75]
	v_mfma_f32_16x16x32_bf16 v[76:79], v[92:95], v[0:3], v[240:243]
	v_mfma_f32_16x16x32_bf16 v[72:75], v[176:179], v[8:11], v[72:75]
	s_waitcnt lgkmcnt(9)
	v_mfma_f32_16x16x32_bf16 v[84:87], v[184:187], v[12:15], v[72:75]
	ds_read_b64_tr_b16 v[88:89], v136 offset:49152
	ds_read_b64_tr_b16 v[90:91], v137 offset:49152
	ds_read_b64_tr_b16 v[98:99], v137 offset:57344
	ds_read_b64_tr_b16 v[96:97], v136 offset:57344
	ds_read_b64_tr_b16 v[92:93], v139 offset:49152
	ds_read_b64_tr_b16 v[94:95], v145 offset:49152
	v_mfma_f32_16x16x32_bf16 v[72:75], v[152:155], v[4:7], v[76:79]
	v_mfma_f32_16x16x32_bf16 v[72:75], v[180:183], v[8:11], v[72:75]
	v_mfma_f32_16x16x32_bf16 v[80:83], v[188:191], v[12:15], v[72:75]
	s_nop 6
	v_mfma_f32_16x16x32_bf16 v[72:75], v[192:195], v[0:3], v[240:243]
	v_mfma_f32_16x16x32_bf16 v[72:75], v[200:203], v[4:7], v[72:75]
	s_waitcnt lgkmcnt(9)
	v_mfma_f32_16x16x32_bf16 v[72:75], v[208:211], v[8:11], v[72:75]
	ds_read_b64_tr_b16 v[178:179], v145 offset:57344
	ds_read_b64_tr_b16 v[176:177], v139 offset:57344
	ds_read_b64_tr_b16 v[184:185], v140 offset:49152
	ds_read_b64_tr_b16 v[186:187], v147 offset:49152
	ds_read_b64_tr_b16 v[154:155], v147 offset:57344
	ds_read_b64_tr_b16 v[152:153], v140 offset:57344
	v_mfma_f32_16x16x32_bf16 v[76:79], v[216:219], v[12:15], v[72:75]
	v_mfma_f32_16x16x32_bf16 v[72:75], v[196:199], v[0:3], v[240:243]
	v_mfma_f32_16x16x32_bf16 v[72:75], v[204:207], v[4:7], v[72:75]
	s_waitcnt lgkmcnt(10)
	v_mfma_f32_16x16x32_bf16 v[60:63], v[224:227], v[68:71], v[60:63]
	ds_read_b64_tr_b16 v[180:181], v148 offset:49152
	ds_read_b64_tr_b16 v[182:183], v149 offset:49152
	ds_read_b64_tr_b16 v[190:191], v149 offset:57344
	ds_read_b64_tr_b16 v[188:189], v148 offset:57344
	ds_read_b64_tr_b16 v[192:193], v133 offset:49152
	v_mfma_f32_16x16x32_bf16 v[60:63], v[228:231], v[64:67], v[60:63]
	v_mfma_f32_16x16x32_bf16 v[52:55], v[88:91], v[68:71], v[52:55]
	s_waitcnt lgkmcnt(9)
	v_mfma_f32_16x16x32_bf16 v[52:55], v[96:99], v[64:67], v[52:55]
	ds_read_b64_tr_b16 v[194:195], v134 offset:49152
	ds_read_b64_tr_b16 v[202:203], v134 offset:57344
	ds_read_b64_tr_b16 v[200:201], v133 offset:57344
	ds_read_b64_tr_b16 v[208:209], v135 offset:49152
	ds_read_b64_tr_b16 v[210:211], v138 offset:49152
	ds_read_b64_tr_b16 v[218:219], v138 offset:57344
	v_mfma_f32_16x16x32_bf16 v[48:51], v[92:95], v[68:71], v[48:51]
	v_mfma_f32_16x16x32_bf16 v[48:51], v[176:179], v[64:67], v[48:51]
	s_waitcnt lgkmcnt(9)
	v_mfma_f32_16x16x32_bf16 v[56:59], v[184:187], v[68:71], v[56:59]
	ds_read_b64_tr_b16 v[216:217], v135 offset:57344
	ds_read_b64_tr_b16 v[196:197], v141 offset:49152
	ds_read_b64_tr_b16 v[198:199], v143 offset:49152
	ds_read_b64_tr_b16 v[206:207], v143 offset:57344
	ds_read_b64_tr_b16 v[204:205], v141 offset:57344
	v_mfma_f32_16x16x32_bf16 v[56:59], v[152:155], v[64:67], v[56:59]
	v_mfma_f32_16x16x32_bf16 v[32:35], v[180:183], v[68:71], v[32:35]
	s_waitcnt lgkmcnt(8)
	v_mfma_f32_16x16x32_bf16 v[32:35], v[188:191], v[64:67], v[32:35]
	v_mfma_f32_16x16x32_bf16 v[36:39], v[192:195], v[68:71], v[36:39]
	v_mfma_f32_16x16x32_bf16 v[36:39], v[200:203], v[64:67], v[36:39]
	s_waitcnt lgkmcnt(2)
	v_mfma_f32_16x16x32_bf16 v[40:43], v[208:211], v[68:71], v[40:43]
	v_mfma_f32_16x16x32_bf16 v[40:43], v[216:219], v[64:67], v[40:43]
	v_mfma_f32_16x16x32_bf16 v[72:75], v[212:215], v[8:11], v[72:75]
	v_mfma_f32_16x16x32_bf16 v[44:47], v[196:199], v[68:71], v[44:47]
	v_mfma_f32_16x16x32_bf16 v[72:75], v[220:223], v[12:15], v[72:75]
	s_waitcnt lgkmcnt(0)
	v_mfma_f32_16x16x32_bf16 v[44:47], v[204:207], v[64:67], v[44:47]
	s_cbranch_vccnz .LBB0_530
	v_add_u32_e32 v64, 0, v109
	s_waitcnt vmcnt(3)
	ds_write_b128 v100, v[16:19] offset:16384
	s_waitcnt vmcnt(2)
	ds_write_b128 v124, v[20:23] offset:16384
	s_waitcnt vmcnt(1)
	ds_write_b128 v64, v[24:27] offset:32768
	v_add_u32_e32 v64, 0, v112
	s_waitcnt vmcnt(0)
	ds_write_b128 v64, v[28:31] offset:32768

.LBB0_536:
	ds_read_b128 v[168:171], v129 offset:16384
	ds_read_b128 v[172:175], v130 offset:16384
	ds_read_b128 v[176:179], v131 offset:16384
	ds_read_b128 v[180:183], v129 offset:17408
	ds_read_b128 v[184:187], v132 offset:16384
	ds_read_b128 v[188:191], v130 offset:17408
	ds_read_b128 v[192:195], v131 offset:17408
	ds_read_b128 v[196:199], v129 offset:24576
	ds_read_b128 v[200:203], v132 offset:17408
	ds_read_b128 v[204:207], v130 offset:24576
	ds_read_b128 v[208:211], v131 offset:24576
	ds_read_b128 v[212:215], v129 offset:25600
	ds_read_b128 v[216:219], v132 offset:24576
	ds_read_b128 v[220:223], v130 offset:25600
	ds_read_b128 v[224:227], v131 offset:25600
	v_sub_f32_e32 v64, v84, v96
	v_exp_f32_e32 v96, v64
	v_sub_f32_e32 v64, v85, v97
	v_exp_f32_e32 v97, v64
	v_sub_f32_e32 v64, v86, v98
	v_exp_f32_e32 v98, v64
	v_sub_f32_e32 v64, v87, v99
	v_exp_f32_e32 v99, v64
	v_sub_f32_e32 v64, v80, v92
	v_exp_f32_e32 v153, v64
	v_sub_f32_e32 v64, v81, v93
	v_exp_f32_e32 v154, v64
	v_sub_f32_e32 v64, v82, v94
	v_exp_f32_e32 v155, v64
	v_sub_f32_e32 v64, v83, v95
	s_waitcnt lgkmcnt(10)
	v_mfma_f32_16x16x32_bf16 v[84:87], v[168:171], v[0:3], v[240:243]
	ds_read_b128 v[228:231], v132 offset:25600
	ds_read_b64_tr_b16 v[168:169], v142 offset:32768
	ds_read_b64_tr_b16 v[170:171], v146 offset:32768
	v_exp_f32_e32 v156, v64
	v_sub_f32_e32 v64, v76, v88
	v_exp_f32_e32 v157, v64
	v_mfma_f32_16x16x32_bf16 v[92:95], v[180:183], v[0:3], v[240:243]
	ds_read_b64_tr_b16 v[182:183], v146 offset:40960
	ds_read_b64_tr_b16 v[180:181], v142 offset:40960
	v_sub_f32_e32 v64, v77, v89
	v_sub_f32_e32 v70, v73, v67
	v_mfma_f32_16x16x32_bf16 v[84:87], v[172:175], v[4:7], v[84:87]
	v_exp_f32_e32 v158, v64
	v_sub_f32_e32 v64, v78, v90
	v_exp_f32_e32 v159, v64
	v_sub_f32_e32 v64, v79, v91
	s_waitcnt lgkmcnt(10)
	v_mfma_f32_16x16x32_bf16 v[88:91], v[188:191], v[4:7], v[92:95]
	ds_read_b64_tr_b16 v[172:173], v136 offset:32768
	ds_read_b64_tr_b16 v[174:175], v137 offset:32768
	ds_read_b64_tr_b16 v[190:191], v137 offset:40960
	ds_read_b64_tr_b16 v[188:189], v136 offset:40960
	v_exp_f32_e32 v160, v64
	v_mfma_f32_16x16x32_bf16 v[80:83], v[176:179], v[8:11], v[84:87]
	ds_read_b64_tr_b16 v[176:177], v139 offset:32768
	v_sub_f32_e32 v64, v72, v66
	v_exp_f32_e32 v161, v64
	v_mfma_f32_16x16x32_bf16 v[76:79], v[192:195], v[8:11], v[88:91]
	v_sub_f32_e32 v68, v74, v68
	s_and_b64 vcc, exec, s[10:11]
	v_mfma_f32_16x16x32_bf16 v[92:95], v[196:199], v[0:3], v[240:243]
	v_mfma_f32_16x16x32_bf16 v[80:83], v[184:187], v[12:15], v[80:83]
	v_exp_f32_e32 v162, v70
	v_exp_f32_e32 v163, v68
	v_mfma_f32_16x16x32_bf16 v[76:79], v[200:203], v[12:15], v[76:79]
	v_mfma_f32_16x16x32_bf16 v[88:91], v[204:207], v[4:7], v[92:95]
	v_sub_f32_e32 v68, v75, v69
	s_waitcnt lgkmcnt(10)
	v_mfma_f32_16x16x32_bf16 v[84:87], v[208:211], v[8:11], v[88:91]
	ds_read_b64_tr_b16 v[178:179], v145 offset:32768
	ds_read_b64_tr_b16 v[194:195], v145 offset:40960
	ds_read_b64_tr_b16 v[192:193], v139 offset:40960
	ds_read_b64_tr_b16 v[196:197], v140 offset:32768
	ds_read_b64_tr_b16 v[198:199], v147 offset:32768
	v_cvt_pk_bf16_f32 v92, v96, v97
	v_cvt_pk_bf16_f32 v93, v98, v99
	v_cvt_pk_bf16_f32 v94, v153, v154
	v_mfma_f32_16x16x32_bf16 v[64:67], v[216:219], v[12:15], v[84:87]
	v_cvt_pk_bf16_f32 v95, v155, v156
	v_mfma_f32_16x16x32_bf16 v[84:87], v[212:215], v[0:3], v[240:243]
	v_exp_f32_e32 v164, v68
	v_mfma_f32_16x16x32_bf16 v[84:87], v[220:223], v[4:7], v[84:87]
	v_mfma_f32_16x16x32_bf16 v[68:71], v[224:227], v[8:11], v[84:87]
	s_nop 6
	v_cvt_pk_bf16_f32 v84, v157, v158
	s_waitcnt lgkmcnt(10)
	v_mfma_f32_16x16x32_bf16 v[68:71], v[228:231], v[12:15], v[68:71]
	ds_read_b64_tr_b16 v[186:187], v147 offset:40960
	ds_read_b64_tr_b16 v[184:185], v140 offset:40960
	ds_read_b64_tr_b16 v[200:201], v148 offset:32768
	ds_read_b64_tr_b16 v[202:203], v149 offset:32768
	ds_read_b64_tr_b16 v[206:207], v149 offset:40960
	v_cvt_pk_bf16_f32 v85, v159, v160
	v_cvt_pk_bf16_f32 v86, v161, v162
	v_mfma_f32_16x16x32_bf16 v[60:63], v[168:171], v[92:95], v[60:63]
	v_cvt_pk_bf16_f32 v87, v163, v164
	s_nop 1
	v_mfma_f32_16x16x32_bf16 v[60:63], v[180:183], v[84:87], v[60:63]
	s_waitcnt lgkmcnt(9)
	v_mfma_f32_16x16x32_bf16 v[52:55], v[172:175], v[92:95], v[52:55]
	ds_read_b64_tr_b16 v[204:205], v148 offset:40960
	ds_read_b64_tr_b16 v[208:209], v133 offset:32768
	ds_read_b64_tr_b16 v[210:211], v134 offset:32768
	ds_read_b64_tr_b16 v[218:219], v134 offset:40960
	ds_read_b64_tr_b16 v[216:217], v133 offset:40960
	ds_read_b64_tr_b16 v[212:213], v135 offset:32768
	v_mfma_f32_16x16x32_bf16 v[52:55], v[188:191], v[84:87], v[52:55]
	v_mfma_f32_16x16x32_bf16 v[48:51], v[176:179], v[92:95], v[48:51]
	s_waitcnt lgkmcnt(9)
	v_mfma_f32_16x16x32_bf16 v[48:51], v[192:195], v[84:87], v[48:51]
	ds_read_b64_tr_b16 v[214:215], v138 offset:32768
	ds_read_b64_tr_b16 v[222:223], v138 offset:40960
	ds_read_b64_tr_b16 v[220:221], v135 offset:40960
	ds_read_b64_tr_b16 v[224:225], v141 offset:32768
	ds_read_b64_tr_b16 v[226:227], v143 offset:32768
	ds_read_b64_tr_b16 v[230:231], v143 offset:40960
	v_mfma_f32_16x16x32_bf16 v[56:59], v[196:199], v[92:95], v[56:59]
	v_mfma_f32_16x16x32_bf16 v[56:59], v[184:187], v[84:87], v[56:59]
	s_waitcnt lgkmcnt(9)
	v_mfma_f32_16x16x32_bf16 v[32:35], v[200:203], v[92:95], v[32:35]
	ds_read_b64_tr_b16 v[228:229], v141 offset:40960
	v_mfma_f32_16x16x32_bf16 v[32:35], v[204:207], v[84:87], v[32:35]
	v_mfma_f32_16x16x32_bf16 v[36:39], v[208:211], v[92:95], v[36:39]
	s_waitcnt lgkmcnt(4)
	v_mfma_f32_16x16x32_bf16 v[36:39], v[216:219], v[84:87], v[36:39]
	v_mfma_f32_16x16x32_bf16 v[40:43], v[212:215], v[92:95], v[40:43]
	v_mfma_f32_16x16x32_bf16 v[40:43], v[220:223], v[84:87], v[40:43]
	s_waitcnt lgkmcnt(0)
	v_mfma_f32_16x16x32_bf16 v[44:47], v[224:227], v[92:95], v[44:47]
	v_mfma_f32_16x16x32_bf16 v[44:47], v[228:231], v[84:87], v[44:47]
	s_cbranch_vccnz .LBB0_538
	v_add_u32_e32 v72, 0, v109
	s_waitcnt vmcnt(3)
	ds_write_b128 v100, v[16:19]
	s_waitcnt vmcnt(2)
	ds_write_b128 v124, v[20:23]
	s_waitcnt vmcnt(1)
	ds_write_b128 v72, v[24:27] offset:49152
	v_add_u32_e32 v72, 0, v112
	s_waitcnt vmcnt(0)
	ds_write_b128 v72, v[28:31] offset:49152

.LBB0_567:
	ds_read_b128 v[88:91], v129
	ds_read_b128 v[92:95], v129 offset:1024
	ds_read_b128 v[96:99], v130
	ds_read_b128 v[152:155], v130 offset:1024
	ds_read_b128 v[172:175], v131
	ds_read_b128 v[176:179], v131 offset:1024
	ds_read_b128 v[180:183], v132
	ds_read_b128 v[184:187], v132 offset:1024
	ds_read_b128 v[188:191], v129 offset:8192
	ds_read_b128 v[192:195], v129 offset:9216
	ds_read_b128 v[196:199], v130 offset:8192
	ds_read_b128 v[200:203], v130 offset:9216
	ds_read_b128 v[204:207], v131 offset:8192
	ds_read_b128 v[208:211], v131 offset:9216
	ds_read_b128 v[212:215], v132 offset:8192
	s_and_b64 vcc, exec, s[10:11]
	s_waitcnt lgkmcnt(10)
	v_mfma_f32_16x16x32_bf16 v[72:75], v[88:91], v[0:3], v[240:243]
	ds_read_b128 v[216:219], v132 offset:9216
	ds_read_b64_tr_b16 v[220:221], v146 offset:49152
	ds_read_b64_tr_b16 v[222:223], v148 offset:49152
	ds_read_b64_tr_b16 v[226:227], v148 offset:57344
	ds_read_b64_tr_b16 v[224:225], v146 offset:57344
	v_mfma_f32_16x16x32_bf16 v[72:75], v[96:99], v[4:7], v[72:75]
	v_mfma_f32_16x16x32_bf16 v[76:79], v[92:95], v[0:3], v[240:243]
	v_mfma_f32_16x16x32_bf16 v[72:75], v[172:175], v[8:11], v[72:75]
	s_waitcnt lgkmcnt(9)
	v_mfma_f32_16x16x32_bf16 v[84:87], v[180:183], v[12:15], v[72:75]
	ds_read_b64_tr_b16 v[228:229], v139 offset:49152
	ds_read_b64_tr_b16 v[230:231], v142 offset:49152
	ds_read_b64_tr_b16 v[90:91], v142 offset:57344
	ds_read_b64_tr_b16 v[88:89], v139 offset:57344
	ds_read_b64_tr_b16 v[96:97], v141 offset:49152
	ds_read_b64_tr_b16 v[98:99], v145 offset:49152
	v_mfma_f32_16x16x32_bf16 v[72:75], v[152:155], v[4:7], v[76:79]
	v_mfma_f32_16x16x32_bf16 v[72:75], v[176:179], v[8:11], v[72:75]
	v_mfma_f32_16x16x32_bf16 v[80:83], v[184:187], v[12:15], v[72:75]
	s_nop 6
	v_mfma_f32_16x16x32_bf16 v[72:75], v[188:191], v[0:3], v[240:243]
	v_mfma_f32_16x16x32_bf16 v[72:75], v[196:199], v[4:7], v[72:75]
	s_waitcnt lgkmcnt(9)
	v_mfma_f32_16x16x32_bf16 v[72:75], v[204:207], v[8:11], v[72:75]
	ds_read_b64_tr_b16 v[94:95], v145 offset:57344
	ds_read_b64_tr_b16 v[92:93], v141 offset:57344
	ds_read_b64_tr_b16 v[172:173], v140 offset:49152
	ds_read_b64_tr_b16 v[174:175], v143 offset:49152
	ds_read_b64_tr_b16 v[182:183], v143 offset:57344
	ds_read_b64_tr_b16 v[180:181], v140 offset:57344
	v_mfma_f32_16x16x32_bf16 v[76:79], v[212:215], v[12:15], v[72:75]
	v_mfma_f32_16x16x32_bf16 v[72:75], v[192:195], v[0:3], v[240:243]
	v_mfma_f32_16x16x32_bf16 v[72:75], v[200:203], v[4:7], v[72:75]
	s_waitcnt lgkmcnt(10)
	v_mfma_f32_16x16x32_bf16 v[60:63], v[220:223], v[68:71], v[60:63]
	ds_read_b64_tr_b16 v[152:153], v147 offset:49152
	ds_read_b64_tr_b16 v[154:155], v149 offset:49152
	ds_read_b64_tr_b16 v[178:179], v149 offset:57344
	ds_read_b64_tr_b16 v[176:177], v147 offset:57344
	ds_read_b64_tr_b16 v[184:185], v133 offset:49152
	v_mfma_f32_16x16x32_bf16 v[60:63], v[224:227], v[64:67], v[60:63]
	v_mfma_f32_16x16x32_bf16 v[56:59], v[228:231], v[68:71], v[56:59]
	s_waitcnt lgkmcnt(9)
	v_mfma_f32_16x16x32_bf16 v[56:59], v[88:91], v[64:67], v[56:59]
	ds_read_b64_tr_b16 v[186:187], v134 offset:49152
	ds_read_b64_tr_b16 v[190:191], v134 offset:57344
	ds_read_b64_tr_b16 v[188:189], v133 offset:57344
	ds_read_b64_tr_b16 v[196:197], v135 offset:49152
	ds_read_b64_tr_b16 v[198:199], v136 offset:49152
	ds_read_b64_tr_b16 v[206:207], v136 offset:57344
	v_mfma_f32_16x16x32_bf16 v[52:55], v[96:99], v[68:71], v[52:55]
	v_mfma_f32_16x16x32_bf16 v[52:55], v[92:95], v[64:67], v[52:55]
	s_waitcnt lgkmcnt(9)
	v_mfma_f32_16x16x32_bf16 v[48:51], v[172:175], v[68:71], v[48:51]
	ds_read_b64_tr_b16 v[204:205], v135 offset:57344
	ds_read_b64_tr_b16 v[212:213], v137 offset:49152
	ds_read_b64_tr_b16 v[214:215], v138 offset:49152
	ds_read_b64_tr_b16 v[194:195], v138 offset:57344
	ds_read_b64_tr_b16 v[192:193], v137 offset:57344
	v_mfma_f32_16x16x32_bf16 v[48:51], v[180:183], v[64:67], v[48:51]
	v_mfma_f32_16x16x32_bf16 v[32:35], v[152:155], v[68:71], v[32:35]
	s_waitcnt lgkmcnt(8)
	v_mfma_f32_16x16x32_bf16 v[32:35], v[176:179], v[64:67], v[32:35]
	v_mfma_f32_16x16x32_bf16 v[36:39], v[184:187], v[68:71], v[36:39]
	v_mfma_f32_16x16x32_bf16 v[36:39], v[188:191], v[64:67], v[36:39]
	s_waitcnt lgkmcnt(2)
	v_mfma_f32_16x16x32_bf16 v[40:43], v[196:199], v[68:71], v[40:43]
	v_mfma_f32_16x16x32_bf16 v[40:43], v[204:207], v[64:67], v[40:43]
	v_mfma_f32_16x16x32_bf16 v[72:75], v[208:211], v[8:11], v[72:75]
	v_mfma_f32_16x16x32_bf16 v[44:47], v[212:215], v[68:71], v[44:47]
	v_mfma_f32_16x16x32_bf16 v[72:75], v[216:219], v[12:15], v[72:75]
	s_waitcnt lgkmcnt(0)
	v_mfma_f32_16x16x32_bf16 v[44:47], v[192:195], v[64:67], v[44:47]
	s_cbranch_vccnz .LBB0_569
	v_add_u32_e32 v64, 0, v109
	s_waitcnt vmcnt(3)
	ds_write_b128 v100, v[16:19] offset:16384
	s_waitcnt vmcnt(2)
	ds_write_b128 v124, v[20:23] offset:16384
	s_waitcnt vmcnt(1)
	ds_write_b128 v64, v[24:27] offset:32768
	v_add_u32_e32 v64, 0, v112
	s_waitcnt vmcnt(0)
	ds_write_b128 v64, v[28:31] offset:32768

.LBB0_575:
	ds_read_b128 v[164:167], v129 offset:16384
	ds_read_b128 v[168:171], v130 offset:16384
	ds_read_b128 v[172:175], v131 offset:16384
	ds_read_b128 v[176:179], v129 offset:17408
	ds_read_b128 v[180:183], v132 offset:16384
	ds_read_b128 v[184:187], v130 offset:17408
	ds_read_b128 v[188:191], v131 offset:17408
	ds_read_b128 v[192:195], v129 offset:24576
	ds_read_b128 v[196:199], v132 offset:17408
	ds_read_b128 v[200:203], v130 offset:24576
	ds_read_b128 v[204:207], v131 offset:24576
	ds_read_b128 v[208:211], v129 offset:25600
	ds_read_b128 v[212:215], v132 offset:24576
	ds_read_b128 v[216:219], v130 offset:25600
	ds_read_b128 v[220:223], v131 offset:25600
	v_sub_f32_e32 v64, v84, v96
	v_exp_f32_e32 v96, v64
	v_sub_f32_e32 v64, v85, v97
	v_exp_f32_e32 v97, v64
	v_sub_f32_e32 v64, v86, v98
	v_exp_f32_e32 v98, v64
	v_sub_f32_e32 v64, v87, v99
	v_exp_f32_e32 v99, v64
	v_sub_f32_e32 v64, v80, v92
	v_exp_f32_e32 v152, v64
	v_sub_f32_e32 v64, v81, v93
	v_exp_f32_e32 v153, v64
	v_sub_f32_e32 v64, v82, v94
	v_exp_f32_e32 v154, v64
	v_sub_f32_e32 v64, v83, v95
	s_waitcnt lgkmcnt(10)
	v_mfma_f32_16x16x32_bf16 v[84:87], v[164:167], v[0:3], v[240:243]
	ds_read_b128 v[224:227], v132 offset:25600
	ds_read_b64_tr_b16 v[228:229], v146 offset:32768
	ds_read_b64_tr_b16 v[230:231], v148 offset:32768
	ds_read_b64_tr_b16 v[166:167], v148 offset:40960
	ds_read_b64_tr_b16 v[164:165], v146 offset:40960
	v_exp_f32_e32 v155, v64
	v_sub_f32_e32 v64, v76, v88
	v_mfma_f32_16x16x32_bf16 v[84:87], v[168:171], v[4:7], v[84:87]
	v_exp_f32_e32 v156, v64
	v_sub_f32_e32 v64, v77, v89
	v_mfma_f32_16x16x32_bf16 v[92:95], v[176:179], v[0:3], v[240:243]
	v_exp_f32_e32 v157, v64
	v_sub_f32_e32 v64, v78, v90
	v_exp_f32_e32 v158, v64
	v_sub_f32_e32 v64, v79, v91
	s_waitcnt lgkmcnt(10)
	v_mfma_f32_16x16x32_bf16 v[88:91], v[184:187], v[4:7], v[92:95]
	ds_read_b64_tr_b16 v[168:169], v139 offset:32768
	ds_read_b64_tr_b16 v[170:171], v142 offset:32768
	ds_read_b64_tr_b16 v[178:179], v142 offset:40960
	ds_read_b64_tr_b16 v[176:177], v139 offset:40960
	ds_read_b64_tr_b16 v[184:185], v141 offset:32768
	v_exp_f32_e32 v159, v64
	v_mfma_f32_16x16x32_bf16 v[80:83], v[172:175], v[8:11], v[84:87]
	v_sub_f32_e32 v64, v72, v66
	v_sub_f32_e32 v70, v73, v67
	v_mfma_f32_16x16x32_bf16 v[76:79], v[188:191], v[8:11], v[88:91]
	v_sub_f32_e32 v68, v74, v68
	s_and_b64 vcc, exec, s[10:11]
	v_mfma_f32_16x16x32_bf16 v[92:95], v[192:195], v[0:3], v[240:243]
	v_mfma_f32_16x16x32_bf16 v[76:79], v[196:199], v[12:15], v[76:79]
	v_mfma_f32_16x16x32_bf16 v[88:91], v[200:203], v[4:7], v[92:95]
	v_mfma_f32_16x16x32_bf16 v[80:83], v[180:183], v[12:15], v[80:83]
	v_exp_f32_e32 v160, v64
	v_exp_f32_e32 v161, v70
	s_waitcnt lgkmcnt(10)
	v_mfma_f32_16x16x32_bf16 v[84:87], v[204:207], v[8:11], v[88:91]
	ds_read_b64_tr_b16 v[186:187], v145 offset:32768
	ds_read_b64_tr_b16 v[174:175], v145 offset:40960
	ds_read_b64_tr_b16 v[172:173], v141 offset:40960
	ds_read_b64_tr_b16 v[188:189], v140 offset:32768
	ds_read_b64_tr_b16 v[190:191], v143 offset:32768
	v_exp_f32_e32 v162, v68
	v_mfma_f32_16x16x32_bf16 v[64:67], v[212:215], v[12:15], v[84:87]
	v_sub_f32_e32 v68, v75, v69
	v_exp_f32_e32 v163, v68
	v_mfma_f32_16x16x32_bf16 v[84:87], v[208:211], v[0:3], v[240:243]
	v_cvt_pk_bf16_f32 v92, v96, v97
	v_cvt_pk_bf16_f32 v93, v98, v99
	v_mfma_f32_16x16x32_bf16 v[84:87], v[216:219], v[4:7], v[84:87]
	v_cvt_pk_bf16_f32 v94, v152, v153
	v_cvt_pk_bf16_f32 v95, v154, v155
	v_mfma_f32_16x16x32_bf16 v[68:71], v[220:223], v[8:11], v[84:87]
	s_nop 4
	v_cvt_pk_bf16_f32 v84, v156, v157
	s_waitcnt lgkmcnt(10)
	v_mfma_f32_16x16x32_bf16 v[68:71], v[224:227], v[12:15], v[68:71]
	ds_read_b64_tr_b16 v[194:195], v143 offset:40960
	ds_read_b64_tr_b16 v[192:193], v140 offset:40960
	ds_read_b64_tr_b16 v[196:197], v147 offset:32768
	ds_read_b64_tr_b16 v[198:199], v149 offset:32768
	ds_read_b64_tr_b16 v[202:203], v149 offset:40960
	v_cvt_pk_bf16_f32 v85, v158, v159
	v_cvt_pk_bf16_f32 v86, v160, v161
	v_mfma_f32_16x16x32_bf16 v[60:63], v[228:231], v[92:95], v[60:63]
	v_cvt_pk_bf16_f32 v87, v162, v163
	s_nop 1
	v_mfma_f32_16x16x32_bf16 v[60:63], v[164:167], v[84:87], v[60:63]
	s_waitcnt lgkmcnt(9)
	v_mfma_f32_16x16x32_bf16 v[56:59], v[168:171], v[92:95], v[56:59]
	ds_read_b64_tr_b16 v[200:201], v147 offset:40960
	ds_read_b64_tr_b16 v[180:181], v133 offset:32768
	ds_read_b64_tr_b16 v[182:183], v134 offset:32768
	ds_read_b64_tr_b16 v[206:207], v134 offset:40960
	ds_read_b64_tr_b16 v[204:205], v133 offset:40960
	ds_read_b64_tr_b16 v[212:213], v135 offset:32768
	v_mfma_f32_16x16x32_bf16 v[56:59], v[176:179], v[84:87], v[56:59]
	v_mfma_f32_16x16x32_bf16 v[52:55], v[184:187], v[92:95], v[52:55]
	s_waitcnt lgkmcnt(9)
	v_mfma_f32_16x16x32_bf16 v[52:55], v[172:175], v[84:87], v[52:55]
	ds_read_b64_tr_b16 v[214:215], v136 offset:32768
	ds_read_b64_tr_b16 v[210:211], v136 offset:40960
	ds_read_b64_tr_b16 v[208:209], v135 offset:40960
	ds_read_b64_tr_b16 v[216:217], v137 offset:32768
	ds_read_b64_tr_b16 v[218:219], v138 offset:32768
	ds_read_b64_tr_b16 v[222:223], v138 offset:40960
	v_mfma_f32_16x16x32_bf16 v[48:51], v[188:191], v[92:95], v[48:51]
	v_mfma_f32_16x16x32_bf16 v[48:51], v[192:195], v[84:87], v[48:51]
	s_waitcnt lgkmcnt(9)
	v_mfma_f32_16x16x32_bf16 v[32:35], v[196:199], v[92:95], v[32:35]
	ds_read_b64_tr_b16 v[220:221], v137 offset:40960
	v_mfma_f32_16x16x32_bf16 v[32:35], v[200:203], v[84:87], v[32:35]
	v_mfma_f32_16x16x32_bf16 v[36:39], v[180:183], v[92:95], v[36:39]
	s_waitcnt lgkmcnt(4)
	v_mfma_f32_16x16x32_bf16 v[36:39], v[204:207], v[84:87], v[36:39]
	v_mfma_f32_16x16x32_bf16 v[40:43], v[212:215], v[92:95], v[40:43]
	v_mfma_f32_16x16x32_bf16 v[40:43], v[208:211], v[84:87], v[40:43]
	s_waitcnt lgkmcnt(0)
	v_mfma_f32_16x16x32_bf16 v[44:47], v[216:219], v[92:95], v[44:47]
	v_mfma_f32_16x16x32_bf16 v[44:47], v[220:223], v[84:87], v[44:47]
	s_cbranch_vccnz .LBB0_577
	v_add_u32_e32 v72, 0, v109
	s_waitcnt vmcnt(3)
	ds_write_b128 v100, v[16:19]
	s_waitcnt vmcnt(2)
	ds_write_b128 v124, v[20:23]
	s_waitcnt vmcnt(1)
	ds_write_b128 v72, v[24:27] offset:49152
	v_add_u32_e32 v72, 0, v112
	s_waitcnt vmcnt(0)
	ds_write_b128 v72, v[28:31] offset:49152

.LBB0_639:
	ds_read_b128 v[88:91], v128
	ds_read_b128 v[92:95], v128 offset:1024
	ds_read_b128 v[156:159], v129
	ds_read_b128 v[188:191], v129 offset:1024
	ds_read_b128 v[192:195], v130
	ds_read_b128 v[196:199], v130 offset:1024
	ds_read_b128 v[200:203], v131
	ds_read_b128 v[204:207], v131 offset:1024
	ds_read_b128 v[208:211], v128 offset:8192
	ds_read_b128 v[212:215], v128 offset:9216
	ds_read_b128 v[216:219], v129 offset:8192
	ds_read_b128 v[220:223], v129 offset:9216
	ds_read_b128 v[224:227], v130 offset:8192
	ds_read_b128 v[228:231], v130 offset:9216
	s_and_b64 vcc, exec, s[10:11]
	s_waitcnt lgkmcnt(9)
	v_mfma_f32_16x16x32_bf16 v[72:75], v[88:91], v[0:3], 0
	ds_read_b128 v[88:91], v131 offset:8192
	v_mfma_f32_16x16x32_bf16 v[80:83], v[92:95], v[0:3], 0
	ds_read_b128 v[92:95], v131 offset:9216
	v_mfma_f32_16x16x32_bf16 v[72:75], v[156:159], v[4:7], v[72:75]
	ds_read_b64_tr_b16 v[156:157], v140 offset:49152
	ds_read_b64_tr_b16 v[158:159], v141 offset:49152
	v_mfma_f32_16x16x32_bf16 v[72:75], v[192:195], v[8:11], v[72:75]
	ds_read_b64_tr_b16 v[194:195], v141 offset:57344
	ds_read_b64_tr_b16 v[192:193], v140 offset:57344
	s_waitcnt lgkmcnt(9)
	v_mfma_f32_16x16x32_bf16 v[76:79], v[200:203], v[12:15], v[72:75]
	ds_read_b64_tr_b16 v[200:201], v136 offset:49152
	ds_read_b64_tr_b16 v[202:203], v137 offset:49152
	v_mfma_f32_16x16x32_bf16 v[72:75], v[188:191], v[4:7], v[80:83]
	ds_read_b64_tr_b16 v[190:191], v137 offset:57344
	ds_read_b64_tr_b16 v[188:189], v136 offset:57344
	v_mfma_f32_16x16x32_bf16 v[72:75], v[196:199], v[8:11], v[72:75]
	ds_read_b64_tr_b16 v[196:197], v138 offset:49152
	ds_read_b64_tr_b16 v[198:199], v142 offset:49152
	v_mfma_f32_16x16x32_bf16 v[72:75], v[204:207], v[12:15], v[72:75]
	v_mfma_f32_16x16x32_bf16 v[80:83], v[208:211], v[0:3], 0
	v_mfma_f32_16x16x32_bf16 v[80:83], v[216:219], v[4:7], v[80:83]
	s_waitcnt lgkmcnt(9)
	v_mfma_f32_16x16x32_bf16 v[80:83], v[224:227], v[8:11], v[80:83]
	ds_read_b64_tr_b16 v[206:207], v142 offset:57344
	ds_read_b64_tr_b16 v[204:205], v138 offset:57344
	ds_read_b64_tr_b16 v[208:209], v139 offset:49152
	ds_read_b64_tr_b16 v[210:211], v143 offset:49152
	ds_read_b64_tr_b16 v[218:219], v143 offset:57344
	ds_read_b64_tr_b16 v[216:217], v139 offset:57344
	v_mfma_f32_16x16x32_bf16 v[84:87], v[88:91], v[12:15], v[80:83]
	v_mfma_f32_16x16x32_bf16 v[80:83], v[212:215], v[0:3], 0
	v_mfma_f32_16x16x32_bf16 v[80:83], v[220:223], v[4:7], v[80:83]
	s_waitcnt lgkmcnt(10)
	v_mfma_f32_16x16x32_bf16 v[48:51], v[156:159], v[68:71], v[48:51]
	ds_read_b64_tr_b16 v[224:225], v145 offset:49152
	ds_read_b64_tr_b16 v[226:227], v146 offset:49152
	ds_read_b64_tr_b16 v[90:91], v146 offset:57344
	ds_read_b64_tr_b16 v[88:89], v145 offset:57344
	ds_read_b64_tr_b16 v[212:213], v147 offset:49152
	v_mfma_f32_16x16x32_bf16 v[48:51], v[192:195], v[64:67], v[48:51]
	v_mfma_f32_16x16x32_bf16 v[40:43], v[200:203], v[68:71], v[40:43]
	s_waitcnt lgkmcnt(9)
	v_mfma_f32_16x16x32_bf16 v[40:43], v[188:191], v[64:67], v[40:43]
	ds_read_b64_tr_b16 v[214:215], v148 offset:49152
	ds_read_b64_tr_b16 v[222:223], v148 offset:57344
	ds_read_b64_tr_b16 v[220:221], v147 offset:57344
	ds_read_b64_tr_b16 v[156:157], v149 offset:49152
	ds_read_b64_tr_b16 v[158:159], v150 offset:49152
	ds_read_b64_tr_b16 v[194:195], v150 offset:57344
	v_mfma_f32_16x16x32_bf16 v[44:47], v[196:199], v[68:71], v[44:47]
	v_mfma_f32_16x16x32_bf16 v[44:47], v[204:207], v[64:67], v[44:47]
	s_waitcnt lgkmcnt(9)
	v_mfma_f32_16x16x32_bf16 v[56:59], v[208:211], v[68:71], v[56:59]
	ds_read_b64_tr_b16 v[192:193], v149 offset:57344
	ds_read_b64_tr_b16 v[200:201], v151 offset:49152
	ds_read_b64_tr_b16 v[202:203], v152 offset:49152
	ds_read_b64_tr_b16 v[190:191], v152 offset:57344
	ds_read_b64_tr_b16 v[188:189], v151 offset:57344
	v_mfma_f32_16x16x32_bf16 v[56:59], v[216:219], v[64:67], v[56:59]
	v_mfma_f32_16x16x32_bf16 v[60:63], v[224:227], v[68:71], v[60:63]
	s_waitcnt lgkmcnt(8)
	v_mfma_f32_16x16x32_bf16 v[60:63], v[88:91], v[64:67], v[60:63]
	v_mfma_f32_16x16x32_bf16 v[52:55], v[212:215], v[68:71], v[52:55]
	v_mfma_f32_16x16x32_bf16 v[52:55], v[220:223], v[64:67], v[52:55]
	s_waitcnt lgkmcnt(2)
	v_mfma_f32_16x16x32_bf16 v[32:35], v[156:159], v[68:71], v[32:35]
	v_mfma_f32_16x16x32_bf16 v[32:35], v[192:195], v[64:67], v[32:35]
	v_mfma_f32_16x16x32_bf16 v[80:83], v[228:231], v[8:11], v[80:83]
	v_mfma_f32_16x16x32_bf16 v[36:39], v[200:203], v[68:71], v[36:39]
	v_mfma_f32_16x16x32_bf16 v[80:83], v[92:95], v[12:15], v[80:83]
	s_waitcnt lgkmcnt(0)
	v_mfma_f32_16x16x32_bf16 v[36:39], v[188:191], v[64:67], v[36:39]
	s_cbranch_vccnz .LBB0_641
	s_waitcnt vmcnt(3)
	ds_write_b128 v98, v[16:19] offset:16384
	s_waitcnt vmcnt(2)
	ds_write_b128 v99, v[20:23] offset:16384
	s_waitcnt vmcnt(1)
	ds_write_b128 v100, v[24:27] offset:32768
	s_waitcnt vmcnt(0)
	ds_write_b128 v124, v[28:31] offset:32768

.LBB0_663:
	ds_read_b128 v[176:179], v128 offset:16384
	ds_read_b128 v[180:183], v128 offset:17408
	ds_read_b128 v[188:191], v129 offset:16384
	ds_read_b128 v[192:195], v130 offset:16384
	ds_read_b128 v[196:199], v131 offset:16384
	ds_read_b128 v[200:203], v129 offset:17408
	ds_read_b128 v[204:207], v130 offset:17408
	ds_read_b128 v[208:211], v129 offset:24576
	ds_read_b128 v[212:215], v131 offset:17408
	ds_read_b128 v[216:219], v128 offset:24576
	ds_read_b128 v[220:223], v130 offset:24576
	ds_read_b128 v[224:227], v128 offset:25600
	ds_read_b128 v[228:231], v131 offset:24576
	v_pk_mul_f32 v[184:185], v[66:67], v[68:69]
	s_waitcnt lgkmcnt(8)
	v_mfma_f32_16x16x32_bf16 v[160:163], v[176:179], v[0:3], 0
	ds_read_b128 v[176:179], v129 offset:25600
	v_mul_f32_e32 v70, v70, v71
	v_mul_f32_e32 v157, v70, v157
	v_mul_f32_e32 v159, v157, v159
	v_mfma_f32_16x16x32_bf16 v[164:167], v[180:183], v[0:3], 0
	ds_read_b128 v[180:183], v130 offset:25600
	v_mul_f32_e32 v186, v153, v159
	v_pk_mul_f32 v[64:65], v[64:65], v[96:97]
	v_pk_mul_f32 v[72:73], v[72:73], v[74:75]
	v_mfma_f32_16x16x32_bf16 v[160:163], v[188:191], v[4:7], v[160:163]
	ds_read_b128 v[188:191], v131 offset:25600
	v_pk_mul_f32 v[96:97], v[64:65], v[186:187] op_sel_hi:[1,0]
	v_pk_mul_f32 v[84:85], v[84:85], v[94:95]
	v_mfma_f32_16x16x32_bf16 v[66:69], v[192:195], v[8:11], v[160:163]
	ds_read_b64_tr_b16 v[192:193], v140 offset:32768
	ds_read_b64_tr_b16 v[194:195], v141 offset:32768
	v_cvt_pk_bf16_f32 v173, v96, v97
	v_pk_mul_f32 v[96:97], v[76:77], v[78:79]
	v_mfma_f32_16x16x32_bf16 v[68:71], v[196:199], v[12:15], v[66:69]
	ds_read_b64_tr_b16 v[198:199], v141 offset:40960
	ds_read_b64_tr_b16 v[196:197], v140 offset:40960
	v_pk_mul_f32 v[96:97], v[96:97], v[186:187] op_sel_hi:[1,0]
	v_pk_mul_f32 v[86:87], v[86:87], v[92:93]
	s_waitcnt lgkmcnt(10)
	v_mfma_f32_16x16x32_bf16 v[164:167], v[200:203], v[4:7], v[164:167]
	ds_read_b64_tr_b16 v[200:201], v136 offset:32768
	ds_read_b64_tr_b16 v[202:203], v137 offset:32768
	v_mul_f32_e64 v66, v184, v186
	v_mul_f32_e64 v67, v185, v186
	v_pk_mul_f32 v[80:81], v[80:81], v[82:83]
	v_cvt_pk_bf16_f32 v172, v66, v67
	v_mfma_f32_16x16x32_bf16 v[64:67], v[204:207], v[8:11], v[164:167]
	ds_read_b64_tr_b16 v[206:207], v137 offset:40960
	ds_read_b64_tr_b16 v[204:205], v136 offset:40960
	s_and_b64 vcc, exec, s[10:11]
	v_mfma_f32_16x16x32_bf16 v[64:67], v[212:215], v[12:15], v[64:67]
	ds_read_b64_tr_b16 v[212:213], v138 offset:32768
	v_mfma_f32_16x16x32_bf16 v[168:171], v[216:219], v[0:3], 0
	v_cvt_pk_bf16_f32 v174, v96, v97
	v_pk_mul_f32 v[96:97], v[72:73], v[186:187] op_sel_hi:[1,0]
	v_mfma_f32_16x16x32_bf16 v[76:79], v[208:211], v[4:7], v[168:171]
	v_cvt_pk_bf16_f32 v175, v96, v97
	s_waitcnt lgkmcnt(9)
	v_mfma_f32_16x16x32_bf16 v[94:97], v[224:227], v[0:3], 0
	ds_read_b64_tr_b16 v[214:215], v142 offset:32768
	ds_read_b64_tr_b16 v[218:219], v142 offset:40960
	ds_read_b64_tr_b16 v[216:217], v138 offset:40960
	ds_read_b64_tr_b16 v[208:209], v139 offset:32768
	ds_read_b64_tr_b16 v[210:211], v143 offset:32768
	ds_read_b64_tr_b16 v[226:227], v143 offset:40960
	v_mfma_f32_16x16x32_bf16 v[72:75], v[220:223], v[8:11], v[76:79]
	v_mul_f32_e32 v162, v153, v158
	v_pk_mul_f32 v[84:85], v[84:85], v[162:163] op_sel_hi:[1,0]
	v_pk_mul_f32 v[86:87], v[86:87], v[162:163] op_sel_hi:[1,0]
	v_mfma_f32_16x16x32_bf16 v[92:95], v[176:179], v[4:7], v[94:97]
	v_cvt_pk_bf16_f32 v84, v84, v85
	v_cvt_pk_bf16_f32 v85, v86, v87
	v_pk_mul_f32 v[86:87], v[88:89], v[90:91]
	v_mfma_f32_16x16x32_bf16 v[92:95], v[180:183], v[8:11], v[92:95]
	v_pk_mul_f32 v[86:87], v[86:87], v[162:163] op_sel_hi:[1,0]
	v_mfma_f32_16x16x32_bf16 v[76:79], v[188:191], v[12:15], v[92:95]
	v_cvt_pk_bf16_f32 v86, v86, v87
	s_nop 4
	v_pk_mul_f32 v[92:93], v[80:81], v[162:163] op_sel_hi:[1,0]
	s_waitcnt lgkmcnt(9)
	v_mfma_f32_16x16x32_bf16 v[48:51], v[192:195], v[172:175], v[48:51]
	ds_read_b64_tr_b16 v[224:225], v139 offset:40960
	ds_read_b64_tr_b16 v[220:221], v145 offset:32768
	ds_read_b64_tr_b16 v[222:223], v146 offset:32768
	ds_read_b64_tr_b16 v[178:179], v146 offset:40960
	ds_read_b64_tr_b16 v[176:177], v145 offset:40960
	ds_read_b64_tr_b16 v[180:181], v147 offset:32768
	v_cvt_pk_bf16_f32 v87, v92, v93
	v_mfma_f32_16x16x32_bf16 v[40:43], v[200:203], v[172:175], v[40:43]
	s_waitcnt lgkmcnt(9)
	v_mfma_f32_16x16x32_bf16 v[40:43], v[204:207], v[84:87], v[40:43]
	ds_read_b64_tr_b16 v[182:183], v148 offset:32768
	ds_read_b64_tr_b16 v[190:191], v148 offset:40960
	ds_read_b64_tr_b16 v[188:189], v147 offset:40960
	ds_read_b64_tr_b16 v[192:193], v149 offset:32768
	ds_read_b64_tr_b16 v[194:195], v150 offset:32768
	ds_read_b64_tr_b16 v[202:203], v150 offset:40960
	v_mfma_f32_16x16x32_bf16 v[44:47], v[212:215], v[172:175], v[44:47]
	v_mfma_f32_16x16x32_bf16 v[44:47], v[216:219], v[84:87], v[44:47]
	s_waitcnt lgkmcnt(9)
	v_mfma_f32_16x16x32_bf16 v[56:59], v[208:211], v[172:175], v[56:59]
	ds_read_b64_tr_b16 v[200:201], v149 offset:40960
	ds_read_b64_tr_b16 v[204:205], v151 offset:32768
	ds_read_b64_tr_b16 v[206:207], v152 offset:32768
	ds_read_b64_tr_b16 v[214:215], v152 offset:40960
	ds_read_b64_tr_b16 v[212:213], v151 offset:40960
	v_mfma_f32_16x16x32_bf16 v[56:59], v[224:227], v[84:87], v[56:59]
	v_mfma_f32_16x16x32_bf16 v[60:63], v[220:223], v[172:175], v[60:63]
	s_waitcnt lgkmcnt(8)
	v_mfma_f32_16x16x32_bf16 v[60:63], v[176:179], v[84:87], v[60:63]
	v_mfma_f32_16x16x32_bf16 v[52:55], v[180:183], v[172:175], v[52:55]
	v_mfma_f32_16x16x32_bf16 v[52:55], v[188:191], v[84:87], v[52:55]
	s_waitcnt lgkmcnt(2)
	v_mfma_f32_16x16x32_bf16 v[32:35], v[192:195], v[172:175], v[32:35]
	v_mfma_f32_16x16x32_bf16 v[32:35], v[200:203], v[84:87], v[32:35]
	v_mfma_f32_16x16x32_bf16 v[36:39], v[204:207], v[172:175], v[36:39]
	v_mfma_f32_16x16x32_bf16 v[72:75], v[228:231], v[12:15], v[72:75]
	v_mfma_f32_16x16x32_bf16 v[48:51], v[196:199], v[84:87], v[48:51]
	s_waitcnt lgkmcnt(0)
	v_mfma_f32_16x16x32_bf16 v[36:39], v[212:215], v[84:87], v[36:39]
	s_cbranch_vccnz .LBB0_665
	s_waitcnt vmcnt(3)
	ds_write_b128 v98, v[16:19]
	s_waitcnt vmcnt(2)
	ds_write_b128 v99, v[20:23]
	s_waitcnt vmcnt(1)
	ds_write_b128 v100, v[24:27] offset:49152
	s_waitcnt vmcnt(0)
	ds_write_b128 v124, v[28:31] offset:49152

.LBB0_742:
	ds_read_b128 v[88:91], v128
	ds_read_b128 v[92:95], v128 offset:1024
	ds_read_b128 v[156:159], v129
	ds_read_b128 v[188:191], v129 offset:1024
	ds_read_b128 v[192:195], v130
	ds_read_b128 v[196:199], v130 offset:1024
	ds_read_b128 v[200:203], v131
	ds_read_b128 v[204:207], v131 offset:1024
	ds_read_b128 v[208:211], v128 offset:8192
	ds_read_b128 v[212:215], v128 offset:9216
	ds_read_b128 v[216:219], v129 offset:8192
	ds_read_b128 v[220:223], v129 offset:9216
	ds_read_b128 v[224:227], v130 offset:8192
	ds_read_b128 v[228:231], v130 offset:9216
	s_and_b64 vcc, exec, s[10:11]
	s_waitcnt lgkmcnt(9)
	v_mfma_f32_16x16x32_bf16 v[72:75], v[88:91], v[0:3], 0
	ds_read_b128 v[88:91], v131 offset:8192
	v_mfma_f32_16x16x32_bf16 v[80:83], v[92:95], v[0:3], 0
	ds_read_b128 v[92:95], v131 offset:9216
	v_mfma_f32_16x16x32_bf16 v[72:75], v[156:159], v[4:7], v[72:75]
	ds_read_b64_tr_b16 v[156:157], v142 offset:49152
	ds_read_b64_tr_b16 v[158:159], v143 offset:49152
	v_mfma_f32_16x16x32_bf16 v[72:75], v[192:195], v[8:11], v[72:75]
	ds_read_b64_tr_b16 v[194:195], v143 offset:57344
	ds_read_b64_tr_b16 v[192:193], v142 offset:57344
	s_waitcnt lgkmcnt(9)
	v_mfma_f32_16x16x32_bf16 v[76:79], v[200:203], v[12:15], v[72:75]
	ds_read_b64_tr_b16 v[200:201], v136 offset:49152
	ds_read_b64_tr_b16 v[202:203], v139 offset:49152
	v_mfma_f32_16x16x32_bf16 v[72:75], v[188:191], v[4:7], v[80:83]
	ds_read_b64_tr_b16 v[190:191], v139 offset:57344
	ds_read_b64_tr_b16 v[188:189], v136 offset:57344
	v_mfma_f32_16x16x32_bf16 v[72:75], v[196:199], v[8:11], v[72:75]
	ds_read_b64_tr_b16 v[196:197], v138 offset:49152
	ds_read_b64_tr_b16 v[198:199], v141 offset:49152
	v_mfma_f32_16x16x32_bf16 v[72:75], v[204:207], v[12:15], v[72:75]
	v_mfma_f32_16x16x32_bf16 v[80:83], v[208:211], v[0:3], 0
	v_mfma_f32_16x16x32_bf16 v[80:83], v[216:219], v[4:7], v[80:83]
	s_waitcnt lgkmcnt(9)
	v_mfma_f32_16x16x32_bf16 v[80:83], v[224:227], v[8:11], v[80:83]
	ds_read_b64_tr_b16 v[206:207], v141 offset:57344
	ds_read_b64_tr_b16 v[204:205], v138 offset:57344
	ds_read_b64_tr_b16 v[208:209], v137 offset:49152
	ds_read_b64_tr_b16 v[210:211], v140 offset:49152
	ds_read_b64_tr_b16 v[218:219], v140 offset:57344
	ds_read_b64_tr_b16 v[216:217], v137 offset:57344
	v_mfma_f32_16x16x32_bf16 v[84:87], v[88:91], v[12:15], v[80:83]
	v_mfma_f32_16x16x32_bf16 v[80:83], v[212:215], v[0:3], 0
	v_mfma_f32_16x16x32_bf16 v[80:83], v[220:223], v[4:7], v[80:83]
	s_waitcnt lgkmcnt(10)
	v_mfma_f32_16x16x32_bf16 v[60:63], v[156:159], v[64:67], v[60:63]
	ds_read_b64_tr_b16 v[224:225], v145 offset:49152
	ds_read_b64_tr_b16 v[226:227], v146 offset:49152
	ds_read_b64_tr_b16 v[90:91], v146 offset:57344
	ds_read_b64_tr_b16 v[88:89], v145 offset:57344
	ds_read_b64_tr_b16 v[212:213], v147 offset:49152
	v_mfma_f32_16x16x32_bf16 v[60:63], v[192:195], v[68:71], v[60:63]
	v_mfma_f32_16x16x32_bf16 v[52:55], v[200:203], v[64:67], v[52:55]
	s_waitcnt lgkmcnt(9)
	v_mfma_f32_16x16x32_bf16 v[52:55], v[188:191], v[68:71], v[52:55]
	ds_read_b64_tr_b16 v[214:215], v148 offset:49152
	ds_read_b64_tr_b16 v[222:223], v148 offset:57344
	ds_read_b64_tr_b16 v[220:221], v147 offset:57344
	ds_read_b64_tr_b16 v[156:157], v149 offset:49152
	ds_read_b64_tr_b16 v[158:159], v150 offset:49152
	ds_read_b64_tr_b16 v[194:195], v150 offset:57344
	v_mfma_f32_16x16x32_bf16 v[44:47], v[196:199], v[64:67], v[44:47]
	v_mfma_f32_16x16x32_bf16 v[44:47], v[204:207], v[68:71], v[44:47]
	s_waitcnt lgkmcnt(9)
	v_mfma_f32_16x16x32_bf16 v[56:59], v[208:211], v[64:67], v[56:59]
	ds_read_b64_tr_b16 v[192:193], v149 offset:57344
	ds_read_b64_tr_b16 v[200:201], v151 offset:49152
	ds_read_b64_tr_b16 v[202:203], v152 offset:49152
	ds_read_b64_tr_b16 v[190:191], v152 offset:57344
	ds_read_b64_tr_b16 v[188:189], v151 offset:57344
	v_mfma_f32_16x16x32_bf16 v[56:59], v[216:219], v[68:71], v[56:59]
	v_mfma_f32_16x16x32_bf16 v[48:51], v[224:227], v[64:67], v[48:51]
	s_waitcnt lgkmcnt(8)
	v_mfma_f32_16x16x32_bf16 v[48:51], v[88:91], v[68:71], v[48:51]
	v_mfma_f32_16x16x32_bf16 v[40:43], v[212:215], v[64:67], v[40:43]
	v_mfma_f32_16x16x32_bf16 v[40:43], v[220:223], v[68:71], v[40:43]
	s_waitcnt lgkmcnt(2)
	v_mfma_f32_16x16x32_bf16 v[32:35], v[156:159], v[64:67], v[32:35]
	v_mfma_f32_16x16x32_bf16 v[32:35], v[192:195], v[68:71], v[32:35]
	v_mfma_f32_16x16x32_bf16 v[80:83], v[228:231], v[8:11], v[80:83]
	v_mfma_f32_16x16x32_bf16 v[36:39], v[200:203], v[64:67], v[36:39]
	v_mfma_f32_16x16x32_bf16 v[80:83], v[92:95], v[12:15], v[80:83]
	s_waitcnt lgkmcnt(0)
	v_mfma_f32_16x16x32_bf16 v[36:39], v[188:191], v[68:71], v[36:39]
	s_cbranch_vccnz .LBB0_744
	s_waitcnt vmcnt(3)
	ds_write_b128 v98, v[16:19] offset:16384
	s_waitcnt vmcnt(2)
	ds_write_b128 v99, v[20:23] offset:16384
	s_waitcnt vmcnt(1)
	ds_write_b128 v100, v[24:27] offset:32768
	s_waitcnt vmcnt(0)
	ds_write_b128 v124, v[28:31] offset:32768

.LBB0_766:
	ds_read_b128 v[176:179], v128 offset:16384
	ds_read_b128 v[180:183], v128 offset:17408
	ds_read_b128 v[188:191], v129 offset:16384
	ds_read_b128 v[192:195], v130 offset:16384
	ds_read_b128 v[196:199], v131 offset:16384
	ds_read_b128 v[200:203], v129 offset:17408
	ds_read_b128 v[204:207], v130 offset:17408
	ds_read_b128 v[208:211], v129 offset:24576
	ds_read_b128 v[212:215], v131 offset:17408
	ds_read_b128 v[216:219], v128 offset:24576
	ds_read_b128 v[220:223], v130 offset:24576
	ds_read_b128 v[224:227], v128 offset:25600
	ds_read_b128 v[228:231], v131 offset:24576
	v_pk_mul_f32 v[184:185], v[66:67], v[68:69]
	s_waitcnt lgkmcnt(8)
	v_mfma_f32_16x16x32_bf16 v[160:163], v[176:179], v[0:3], 0
	ds_read_b128 v[176:179], v129 offset:25600
	v_mul_f32_e32 v70, v70, v71
	v_mul_f32_e32 v157, v70, v157
	v_mul_f32_e32 v159, v157, v159
	v_mfma_f32_16x16x32_bf16 v[164:167], v[180:183], v[0:3], 0
	ds_read_b128 v[180:183], v130 offset:25600
	v_mul_f32_e32 v186, v153, v159
	v_pk_mul_f32 v[64:65], v[64:65], v[96:97]
	v_pk_mul_f32 v[72:73], v[72:73], v[74:75]
	v_mfma_f32_16x16x32_bf16 v[160:163], v[188:191], v[4:7], v[160:163]
	ds_read_b128 v[188:191], v131 offset:25600
	v_pk_mul_f32 v[96:97], v[64:65], v[186:187] op_sel_hi:[1,0]
	v_pk_mul_f32 v[84:85], v[84:85], v[94:95]
	v_mfma_f32_16x16x32_bf16 v[66:69], v[192:195], v[8:11], v[160:163]
	ds_read_b64_tr_b16 v[192:193], v142 offset:32768
	ds_read_b64_tr_b16 v[194:195], v143 offset:32768
	v_cvt_pk_bf16_f32 v173, v96, v97
	v_pk_mul_f32 v[96:97], v[76:77], v[78:79]
	v_mfma_f32_16x16x32_bf16 v[68:71], v[196:199], v[12:15], v[66:69]
	ds_read_b64_tr_b16 v[198:199], v143 offset:40960
	ds_read_b64_tr_b16 v[196:197], v142 offset:40960
	v_pk_mul_f32 v[96:97], v[96:97], v[186:187] op_sel_hi:[1,0]
	v_pk_mul_f32 v[86:87], v[86:87], v[92:93]
	s_waitcnt lgkmcnt(10)
	v_mfma_f32_16x16x32_bf16 v[164:167], v[200:203], v[4:7], v[164:167]
	ds_read_b64_tr_b16 v[200:201], v136 offset:32768
	ds_read_b64_tr_b16 v[202:203], v139 offset:32768
	v_mul_f32_e64 v66, v184, v186
	v_mul_f32_e64 v67, v185, v186
	v_pk_mul_f32 v[80:81], v[80:81], v[82:83]
	v_cvt_pk_bf16_f32 v172, v66, v67
	v_mfma_f32_16x16x32_bf16 v[64:67], v[204:207], v[8:11], v[164:167]
	ds_read_b64_tr_b16 v[206:207], v139 offset:40960
	ds_read_b64_tr_b16 v[204:205], v136 offset:40960
	s_and_b64 vcc, exec, s[10:11]
	v_mfma_f32_16x16x32_bf16 v[64:67], v[212:215], v[12:15], v[64:67]
	ds_read_b64_tr_b16 v[212:213], v138 offset:32768
	v_mfma_f32_16x16x32_bf16 v[168:171], v[216:219], v[0:3], 0
	v_cvt_pk_bf16_f32 v174, v96, v97
	v_pk_mul_f32 v[96:97], v[72:73], v[186:187] op_sel_hi:[1,0]
	v_mfma_f32_16x16x32_bf16 v[76:79], v[208:211], v[4:7], v[168:171]
	v_cvt_pk_bf16_f32 v175, v96, v97
	s_waitcnt lgkmcnt(9)
	v_mfma_f32_16x16x32_bf16 v[94:97], v[224:227], v[0:3], 0
	ds_read_b64_tr_b16 v[214:215], v141 offset:32768
	ds_read_b64_tr_b16 v[218:219], v141 offset:40960
	ds_read_b64_tr_b16 v[216:217], v138 offset:40960
	ds_read_b64_tr_b16 v[208:209], v137 offset:32768
	ds_read_b64_tr_b16 v[210:211], v140 offset:32768
	ds_read_b64_tr_b16 v[226:227], v140 offset:40960
	v_mfma_f32_16x16x32_bf16 v[72:75], v[220:223], v[8:11], v[76:79]
	v_mul_f32_e32 v162, v153, v158
	v_pk_mul_f32 v[84:85], v[84:85], v[162:163] op_sel_hi:[1,0]
	v_pk_mul_f32 v[86:87], v[86:87], v[162:163] op_sel_hi:[1,0]
	v_mfma_f32_16x16x32_bf16 v[92:95], v[176:179], v[4:7], v[94:97]
	v_cvt_pk_bf16_f32 v84, v84, v85
	v_cvt_pk_bf16_f32 v85, v86, v87
	v_pk_mul_f32 v[86:87], v[88:89], v[90:91]
	v_mfma_f32_16x16x32_bf16 v[92:95], v[180:183], v[8:11], v[92:95]
	v_pk_mul_f32 v[86:87], v[86:87], v[162:163] op_sel_hi:[1,0]
	v_mfma_f32_16x16x32_bf16 v[76:79], v[188:191], v[12:15], v[92:95]
	v_cvt_pk_bf16_f32 v86, v86, v87
	s_nop 4
	v_pk_mul_f32 v[92:93], v[80:81], v[162:163] op_sel_hi:[1,0]
	s_waitcnt lgkmcnt(9)
	v_mfma_f32_16x16x32_bf16 v[60:63], v[192:195], v[172:175], v[60:63]
	ds_read_b64_tr_b16 v[224:225], v137 offset:40960
	ds_read_b64_tr_b16 v[220:221], v145 offset:32768
	ds_read_b64_tr_b16 v[222:223], v146 offset:32768
	ds_read_b64_tr_b16 v[178:179], v146 offset:40960
	ds_read_b64_tr_b16 v[176:177], v145 offset:40960
	ds_read_b64_tr_b16 v[180:181], v147 offset:32768
	v_cvt_pk_bf16_f32 v87, v92, v93
	v_mfma_f32_16x16x32_bf16 v[52:55], v[200:203], v[172:175], v[52:55]
	s_waitcnt lgkmcnt(9)
	v_mfma_f32_16x16x32_bf16 v[52:55], v[204:207], v[84:87], v[52:55]
	ds_read_b64_tr_b16 v[182:183], v148 offset:32768
	ds_read_b64_tr_b16 v[190:191], v148 offset:40960
	ds_read_b64_tr_b16 v[188:189], v147 offset:40960
	ds_read_b64_tr_b16 v[192:193], v149 offset:32768
	ds_read_b64_tr_b16 v[194:195], v150 offset:32768
	ds_read_b64_tr_b16 v[202:203], v150 offset:40960
	v_mfma_f32_16x16x32_bf16 v[44:47], v[212:215], v[172:175], v[44:47]
	v_mfma_f32_16x16x32_bf16 v[44:47], v[216:219], v[84:87], v[44:47]
	s_waitcnt lgkmcnt(9)
	v_mfma_f32_16x16x32_bf16 v[56:59], v[208:211], v[172:175], v[56:59]
	ds_read_b64_tr_b16 v[200:201], v149 offset:40960
	ds_read_b64_tr_b16 v[204:205], v151 offset:32768
	ds_read_b64_tr_b16 v[206:207], v152 offset:32768
	ds_read_b64_tr_b16 v[214:215], v152 offset:40960
	ds_read_b64_tr_b16 v[212:213], v151 offset:40960
	v_mfma_f32_16x16x32_bf16 v[56:59], v[224:227], v[84:87], v[56:59]
	v_mfma_f32_16x16x32_bf16 v[48:51], v[220:223], v[172:175], v[48:51]
	s_waitcnt lgkmcnt(8)
	v_mfma_f32_16x16x32_bf16 v[48:51], v[176:179], v[84:87], v[48:51]
	v_mfma_f32_16x16x32_bf16 v[40:43], v[180:183], v[172:175], v[40:43]
	v_mfma_f32_16x16x32_bf16 v[40:43], v[188:191], v[84:87], v[40:43]
	s_waitcnt lgkmcnt(2)
	v_mfma_f32_16x16x32_bf16 v[32:35], v[192:195], v[172:175], v[32:35]
	v_mfma_f32_16x16x32_bf16 v[32:35], v[200:203], v[84:87], v[32:35]
	v_mfma_f32_16x16x32_bf16 v[36:39], v[204:207], v[172:175], v[36:39]
	v_mfma_f32_16x16x32_bf16 v[72:75], v[228:231], v[12:15], v[72:75]
	v_mfma_f32_16x16x32_bf16 v[60:63], v[196:199], v[84:87], v[60:63]
	s_waitcnt lgkmcnt(0)
	v_mfma_f32_16x16x32_bf16 v[36:39], v[212:215], v[84:87], v[36:39]
	s_cbranch_vccnz .LBB0_768
	s_waitcnt vmcnt(3)
	ds_write_b128 v98, v[16:19]
	s_waitcnt vmcnt(2)
	ds_write_b128 v99, v[20:23]
	s_waitcnt vmcnt(1)
	ds_write_b128 v100, v[24:27] offset:49152
	s_waitcnt vmcnt(0)
	ds_write_b128 v124, v[28:31] offset:49152

.LBB0_1919:
	ds_read_b128 v[88:91], v129
	ds_read_b128 v[92:95], v129 offset:1024
	ds_read_b128 v[96:99], v130
	ds_read_b128 v[152:155], v130 offset:1024
	ds_read_b128 v[176:179], v131
	ds_read_b128 v[180:183], v131 offset:1024
	ds_read_b128 v[184:187], v132
	ds_read_b128 v[188:191], v132 offset:1024
	ds_read_b128 v[192:195], v129 offset:8192
	ds_read_b128 v[196:199], v129 offset:9216
	ds_read_b128 v[200:203], v130 offset:8192
	ds_read_b128 v[204:207], v130 offset:9216
	ds_read_b128 v[208:211], v131 offset:8192
	ds_read_b128 v[212:215], v131 offset:9216
	ds_read_b128 v[216:219], v132 offset:8192
	s_and_b64 vcc, exec, s[6:7]
	s_waitcnt lgkmcnt(10)
	v_mfma_f32_16x16x32_bf16 v[72:75], v[88:91], v[0:3], v[240:243]
	ds_read_b128 v[220:223], v132 offset:9216
	ds_read_b64_tr_b16 v[224:225], v142 offset:49152
	ds_read_b64_tr_b16 v[226:227], v146 offset:49152
	ds_read_b64_tr_b16 v[230:231], v146 offset:57344
	ds_read_b64_tr_b16 v[228:229], v142 offset:57344
	v_mfma_f32_16x16x32_bf16 v[72:75], v[96:99], v[4:7], v[72:75]
	v_mfma_f32_16x16x32_bf16 v[76:79], v[92:95], v[0:3], v[240:243]
	v_mfma_f32_16x16x32_bf16 v[72:75], v[176:179], v[8:11], v[72:75]
	s_waitcnt lgkmcnt(9)
	v_mfma_f32_16x16x32_bf16 v[84:87], v[184:187], v[12:15], v[72:75]
	ds_read_b64_tr_b16 v[88:89], v136 offset:49152
	ds_read_b64_tr_b16 v[90:91], v137 offset:49152
	ds_read_b64_tr_b16 v[98:99], v137 offset:57344
	ds_read_b64_tr_b16 v[96:97], v136 offset:57344
	ds_read_b64_tr_b16 v[92:93], v139 offset:49152
	ds_read_b64_tr_b16 v[94:95], v145 offset:49152
	v_mfma_f32_16x16x32_bf16 v[72:75], v[152:155], v[4:7], v[76:79]
	v_mfma_f32_16x16x32_bf16 v[72:75], v[180:183], v[8:11], v[72:75]
	v_mfma_f32_16x16x32_bf16 v[80:83], v[188:191], v[12:15], v[72:75]
	s_nop 6
	v_mfma_f32_16x16x32_bf16 v[72:75], v[192:195], v[0:3], v[240:243]
	v_mfma_f32_16x16x32_bf16 v[72:75], v[200:203], v[4:7], v[72:75]
	s_waitcnt lgkmcnt(9)
	v_mfma_f32_16x16x32_bf16 v[72:75], v[208:211], v[8:11], v[72:75]
	ds_read_b64_tr_b16 v[178:179], v145 offset:57344
	ds_read_b64_tr_b16 v[176:177], v139 offset:57344
	ds_read_b64_tr_b16 v[184:185], v140 offset:49152
	ds_read_b64_tr_b16 v[186:187], v147 offset:49152
	ds_read_b64_tr_b16 v[154:155], v147 offset:57344
	ds_read_b64_tr_b16 v[152:153], v140 offset:57344
	v_mfma_f32_16x16x32_bf16 v[76:79], v[216:219], v[12:15], v[72:75]
	v_mfma_f32_16x16x32_bf16 v[72:75], v[196:199], v[0:3], v[240:243]
	v_mfma_f32_16x16x32_bf16 v[72:75], v[204:207], v[4:7], v[72:75]
	s_waitcnt lgkmcnt(10)
	v_mfma_f32_16x16x32_bf16 v[60:63], v[224:227], v[68:71], v[60:63]
	ds_read_b64_tr_b16 v[180:181], v148 offset:49152
	ds_read_b64_tr_b16 v[182:183], v149 offset:49152
	ds_read_b64_tr_b16 v[190:191], v149 offset:57344
	ds_read_b64_tr_b16 v[188:189], v148 offset:57344
	ds_read_b64_tr_b16 v[192:193], v133 offset:49152
	v_mfma_f32_16x16x32_bf16 v[60:63], v[228:231], v[64:67], v[60:63]
	v_mfma_f32_16x16x32_bf16 v[52:55], v[88:91], v[68:71], v[52:55]
	s_waitcnt lgkmcnt(9)
	v_mfma_f32_16x16x32_bf16 v[52:55], v[96:99], v[64:67], v[52:55]
	ds_read_b64_tr_b16 v[194:195], v134 offset:49152
	ds_read_b64_tr_b16 v[202:203], v134 offset:57344
	ds_read_b64_tr_b16 v[200:201], v133 offset:57344
	ds_read_b64_tr_b16 v[208:209], v135 offset:49152
	ds_read_b64_tr_b16 v[210:211], v138 offset:49152
	ds_read_b64_tr_b16 v[218:219], v138 offset:57344
	v_mfma_f32_16x16x32_bf16 v[48:51], v[92:95], v[68:71], v[48:51]
	v_mfma_f32_16x16x32_bf16 v[48:51], v[176:179], v[64:67], v[48:51]
	s_waitcnt lgkmcnt(9)
	v_mfma_f32_16x16x32_bf16 v[56:59], v[184:187], v[68:71], v[56:59]
	ds_read_b64_tr_b16 v[216:217], v135 offset:57344
	ds_read_b64_tr_b16 v[196:197], v141 offset:49152
	ds_read_b64_tr_b16 v[198:199], v143 offset:49152
	ds_read_b64_tr_b16 v[206:207], v143 offset:57344
	ds_read_b64_tr_b16 v[204:205], v141 offset:57344
	v_mfma_f32_16x16x32_bf16 v[56:59], v[152:155], v[64:67], v[56:59]
	v_mfma_f32_16x16x32_bf16 v[32:35], v[180:183], v[68:71], v[32:35]
	s_waitcnt lgkmcnt(8)
	v_mfma_f32_16x16x32_bf16 v[32:35], v[188:191], v[64:67], v[32:35]
	v_mfma_f32_16x16x32_bf16 v[36:39], v[192:195], v[68:71], v[36:39]
	v_mfma_f32_16x16x32_bf16 v[36:39], v[200:203], v[64:67], v[36:39]
	s_waitcnt lgkmcnt(2)
	v_mfma_f32_16x16x32_bf16 v[40:43], v[208:211], v[68:71], v[40:43]
	v_mfma_f32_16x16x32_bf16 v[40:43], v[216:219], v[64:67], v[40:43]
	v_mfma_f32_16x16x32_bf16 v[72:75], v[212:215], v[8:11], v[72:75]
	v_mfma_f32_16x16x32_bf16 v[44:47], v[196:199], v[68:71], v[44:47]
	v_mfma_f32_16x16x32_bf16 v[72:75], v[220:223], v[12:15], v[72:75]
	s_waitcnt lgkmcnt(0)
	v_mfma_f32_16x16x32_bf16 v[44:47], v[204:207], v[64:67], v[44:47]
	s_cbranch_vccnz .LBB0_1921
	v_add_u32_e32 v64, 0, v109
	s_waitcnt vmcnt(3)
	ds_write_b128 v100, v[16:19] offset:16384
	s_waitcnt vmcnt(2)
	ds_write_b128 v124, v[20:23] offset:16384
	s_waitcnt vmcnt(1)
	ds_write_b128 v64, v[24:27] offset:32768
	v_add_u32_e32 v64, 0, v112
	s_waitcnt vmcnt(0)
	ds_write_b128 v64, v[28:31] offset:32768

.LBB0_1927:
	ds_read_b128 v[168:171], v129 offset:16384
	ds_read_b128 v[172:175], v130 offset:16384
	ds_read_b128 v[176:179], v131 offset:16384
	ds_read_b128 v[180:183], v129 offset:17408
	ds_read_b128 v[184:187], v132 offset:16384
	ds_read_b128 v[188:191], v130 offset:17408
	ds_read_b128 v[192:195], v131 offset:17408
	ds_read_b128 v[196:199], v129 offset:24576
	ds_read_b128 v[200:203], v132 offset:17408
	ds_read_b128 v[204:207], v130 offset:24576
	ds_read_b128 v[208:211], v131 offset:24576
	ds_read_b128 v[212:215], v129 offset:25600
	ds_read_b128 v[216:219], v132 offset:24576
	ds_read_b128 v[220:223], v130 offset:25600
	ds_read_b128 v[224:227], v131 offset:25600
	v_sub_f32_e32 v64, v84, v96
	v_exp_f32_e32 v96, v64
	v_sub_f32_e32 v64, v85, v97
	v_exp_f32_e32 v97, v64
	v_sub_f32_e32 v64, v86, v98
	v_exp_f32_e32 v98, v64
	v_sub_f32_e32 v64, v87, v99
	v_exp_f32_e32 v99, v64
	v_sub_f32_e32 v64, v80, v92
	v_exp_f32_e32 v153, v64
	v_sub_f32_e32 v64, v81, v93
	v_exp_f32_e32 v154, v64
	v_sub_f32_e32 v64, v82, v94
	v_exp_f32_e32 v155, v64
	v_sub_f32_e32 v64, v83, v95
	s_waitcnt lgkmcnt(10)
	v_mfma_f32_16x16x32_bf16 v[84:87], v[168:171], v[0:3], v[240:243]
	ds_read_b128 v[228:231], v132 offset:25600
	ds_read_b64_tr_b16 v[168:169], v142 offset:32768
	ds_read_b64_tr_b16 v[170:171], v146 offset:32768
	v_exp_f32_e32 v156, v64
	v_sub_f32_e32 v64, v76, v88
	v_exp_f32_e32 v157, v64
	v_mfma_f32_16x16x32_bf16 v[92:95], v[180:183], v[0:3], v[240:243]
	ds_read_b64_tr_b16 v[182:183], v146 offset:40960
	ds_read_b64_tr_b16 v[180:181], v142 offset:40960
	v_sub_f32_e32 v64, v77, v89
	v_sub_f32_e32 v70, v73, v67
	v_mfma_f32_16x16x32_bf16 v[84:87], v[172:175], v[4:7], v[84:87]
	v_exp_f32_e32 v158, v64
	v_sub_f32_e32 v64, v78, v90
	v_exp_f32_e32 v159, v64
	v_sub_f32_e32 v64, v79, v91
	s_waitcnt lgkmcnt(10)
	v_mfma_f32_16x16x32_bf16 v[88:91], v[188:191], v[4:7], v[92:95]
	ds_read_b64_tr_b16 v[172:173], v136 offset:32768
	ds_read_b64_tr_b16 v[174:175], v137 offset:32768
	ds_read_b64_tr_b16 v[190:191], v137 offset:40960
	ds_read_b64_tr_b16 v[188:189], v136 offset:40960
	v_exp_f32_e32 v160, v64
	v_mfma_f32_16x16x32_bf16 v[80:83], v[176:179], v[8:11], v[84:87]
	ds_read_b64_tr_b16 v[176:177], v139 offset:32768
	v_sub_f32_e32 v64, v72, v66
	v_exp_f32_e32 v161, v64
	v_mfma_f32_16x16x32_bf16 v[76:79], v[192:195], v[8:11], v[88:91]
	v_sub_f32_e32 v68, v74, v68
	s_and_b64 vcc, exec, s[6:7]
	v_mfma_f32_16x16x32_bf16 v[92:95], v[196:199], v[0:3], v[240:243]
	v_mfma_f32_16x16x32_bf16 v[80:83], v[184:187], v[12:15], v[80:83]
	v_exp_f32_e32 v162, v70
	v_exp_f32_e32 v163, v68
	v_mfma_f32_16x16x32_bf16 v[76:79], v[200:203], v[12:15], v[76:79]
	v_mfma_f32_16x16x32_bf16 v[88:91], v[204:207], v[4:7], v[92:95]
	v_sub_f32_e32 v68, v75, v69
	s_waitcnt lgkmcnt(10)
	v_mfma_f32_16x16x32_bf16 v[84:87], v[208:211], v[8:11], v[88:91]
	ds_read_b64_tr_b16 v[178:179], v145 offset:32768
	ds_read_b64_tr_b16 v[194:195], v145 offset:40960
	ds_read_b64_tr_b16 v[192:193], v139 offset:40960
	ds_read_b64_tr_b16 v[196:197], v140 offset:32768
	ds_read_b64_tr_b16 v[198:199], v147 offset:32768
	v_cvt_pk_bf16_f32 v92, v96, v97
	v_cvt_pk_bf16_f32 v93, v98, v99
	v_cvt_pk_bf16_f32 v94, v153, v154
	v_mfma_f32_16x16x32_bf16 v[64:67], v[216:219], v[12:15], v[84:87]
	v_cvt_pk_bf16_f32 v95, v155, v156
	v_mfma_f32_16x16x32_bf16 v[84:87], v[212:215], v[0:3], v[240:243]
	v_exp_f32_e32 v164, v68
	v_mfma_f32_16x16x32_bf16 v[84:87], v[220:223], v[4:7], v[84:87]
	v_mfma_f32_16x16x32_bf16 v[68:71], v[224:227], v[8:11], v[84:87]
	s_nop 6
	v_cvt_pk_bf16_f32 v84, v157, v158
	s_waitcnt lgkmcnt(10)
	v_mfma_f32_16x16x32_bf16 v[68:71], v[228:231], v[12:15], v[68:71]
	ds_read_b64_tr_b16 v[186:187], v147 offset:40960
	ds_read_b64_tr_b16 v[184:185], v140 offset:40960
	ds_read_b64_tr_b16 v[200:201], v148 offset:32768
	ds_read_b64_tr_b16 v[202:203], v149 offset:32768
	ds_read_b64_tr_b16 v[206:207], v149 offset:40960
	v_cvt_pk_bf16_f32 v85, v159, v160
	v_cvt_pk_bf16_f32 v86, v161, v162
	v_mfma_f32_16x16x32_bf16 v[60:63], v[168:171], v[92:95], v[60:63]
	v_cvt_pk_bf16_f32 v87, v163, v164
	s_nop 1
	v_mfma_f32_16x16x32_bf16 v[60:63], v[180:183], v[84:87], v[60:63]
	s_waitcnt lgkmcnt(9)
	v_mfma_f32_16x16x32_bf16 v[52:55], v[172:175], v[92:95], v[52:55]
	ds_read_b64_tr_b16 v[204:205], v148 offset:40960
	ds_read_b64_tr_b16 v[208:209], v133 offset:32768
	ds_read_b64_tr_b16 v[210:211], v134 offset:32768
	ds_read_b64_tr_b16 v[218:219], v134 offset:40960
	ds_read_b64_tr_b16 v[216:217], v133 offset:40960
	ds_read_b64_tr_b16 v[212:213], v135 offset:32768
	v_mfma_f32_16x16x32_bf16 v[52:55], v[188:191], v[84:87], v[52:55]
	v_mfma_f32_16x16x32_bf16 v[48:51], v[176:179], v[92:95], v[48:51]
	s_waitcnt lgkmcnt(9)
	v_mfma_f32_16x16x32_bf16 v[48:51], v[192:195], v[84:87], v[48:51]
	ds_read_b64_tr_b16 v[214:215], v138 offset:32768
	ds_read_b64_tr_b16 v[222:223], v138 offset:40960
	ds_read_b64_tr_b16 v[220:221], v135 offset:40960
	ds_read_b64_tr_b16 v[224:225], v141 offset:32768
	ds_read_b64_tr_b16 v[226:227], v143 offset:32768
	ds_read_b64_tr_b16 v[230:231], v143 offset:40960
	v_mfma_f32_16x16x32_bf16 v[56:59], v[196:199], v[92:95], v[56:59]
	v_mfma_f32_16x16x32_bf16 v[56:59], v[184:187], v[84:87], v[56:59]
	s_waitcnt lgkmcnt(9)
	v_mfma_f32_16x16x32_bf16 v[32:35], v[200:203], v[92:95], v[32:35]
	ds_read_b64_tr_b16 v[228:229], v141 offset:40960
	v_mfma_f32_16x16x32_bf16 v[32:35], v[204:207], v[84:87], v[32:35]
	v_mfma_f32_16x16x32_bf16 v[36:39], v[208:211], v[92:95], v[36:39]
	s_waitcnt lgkmcnt(4)
	v_mfma_f32_16x16x32_bf16 v[36:39], v[216:219], v[84:87], v[36:39]
	v_mfma_f32_16x16x32_bf16 v[40:43], v[212:215], v[92:95], v[40:43]
	v_mfma_f32_16x16x32_bf16 v[40:43], v[220:223], v[84:87], v[40:43]
	s_waitcnt lgkmcnt(0)
	v_mfma_f32_16x16x32_bf16 v[44:47], v[224:227], v[92:95], v[44:47]
	v_mfma_f32_16x16x32_bf16 v[44:47], v[228:231], v[84:87], v[44:47]
	s_cbranch_vccnz .LBB0_1929
	v_add_u32_e32 v72, 0, v109
	s_waitcnt vmcnt(3)
	ds_write_b128 v100, v[16:19]
	s_waitcnt vmcnt(2)
	ds_write_b128 v124, v[20:23]
	s_waitcnt vmcnt(1)
	ds_write_b128 v72, v[24:27] offset:49152
	v_add_u32_e32 v72, 0, v112
	s_waitcnt vmcnt(0)
	ds_write_b128 v72, v[28:31] offset:49152

.LBB0_1958:
	ds_read_b128 v[88:91], v129
	ds_read_b128 v[92:95], v129 offset:1024
	ds_read_b128 v[96:99], v130
	ds_read_b128 v[152:155], v130 offset:1024
	ds_read_b128 v[172:175], v131
	ds_read_b128 v[176:179], v131 offset:1024
	ds_read_b128 v[180:183], v132
	ds_read_b128 v[184:187], v132 offset:1024
	ds_read_b128 v[188:191], v129 offset:8192
	ds_read_b128 v[192:195], v129 offset:9216
	ds_read_b128 v[196:199], v130 offset:8192
	ds_read_b128 v[200:203], v130 offset:9216
	ds_read_b128 v[204:207], v131 offset:8192
	ds_read_b128 v[208:211], v131 offset:9216
	ds_read_b128 v[212:215], v132 offset:8192
	s_and_b64 vcc, exec, s[6:7]
	s_waitcnt lgkmcnt(10)
	v_mfma_f32_16x16x32_bf16 v[72:75], v[88:91], v[0:3], v[240:243]
	ds_read_b128 v[216:219], v132 offset:9216
	ds_read_b64_tr_b16 v[220:221], v146 offset:49152
	ds_read_b64_tr_b16 v[222:223], v148 offset:49152
	ds_read_b64_tr_b16 v[226:227], v148 offset:57344
	ds_read_b64_tr_b16 v[224:225], v146 offset:57344
	v_mfma_f32_16x16x32_bf16 v[72:75], v[96:99], v[4:7], v[72:75]
	v_mfma_f32_16x16x32_bf16 v[76:79], v[92:95], v[0:3], v[240:243]
	v_mfma_f32_16x16x32_bf16 v[72:75], v[172:175], v[8:11], v[72:75]
	s_waitcnt lgkmcnt(9)
	v_mfma_f32_16x16x32_bf16 v[84:87], v[180:183], v[12:15], v[72:75]
	ds_read_b64_tr_b16 v[228:229], v139 offset:49152
	ds_read_b64_tr_b16 v[230:231], v142 offset:49152
	ds_read_b64_tr_b16 v[90:91], v142 offset:57344
	ds_read_b64_tr_b16 v[88:89], v139 offset:57344
	ds_read_b64_tr_b16 v[96:97], v141 offset:49152
	ds_read_b64_tr_b16 v[98:99], v145 offset:49152
	v_mfma_f32_16x16x32_bf16 v[72:75], v[152:155], v[4:7], v[76:79]
	v_mfma_f32_16x16x32_bf16 v[72:75], v[176:179], v[8:11], v[72:75]
	v_mfma_f32_16x16x32_bf16 v[80:83], v[184:187], v[12:15], v[72:75]
	s_nop 6
	v_mfma_f32_16x16x32_bf16 v[72:75], v[188:191], v[0:3], v[240:243]
	v_mfma_f32_16x16x32_bf16 v[72:75], v[196:199], v[4:7], v[72:75]
	s_waitcnt lgkmcnt(9)
	v_mfma_f32_16x16x32_bf16 v[72:75], v[204:207], v[8:11], v[72:75]
	ds_read_b64_tr_b16 v[94:95], v145 offset:57344
	ds_read_b64_tr_b16 v[92:93], v141 offset:57344
	ds_read_b64_tr_b16 v[172:173], v140 offset:49152
	ds_read_b64_tr_b16 v[174:175], v143 offset:49152
	ds_read_b64_tr_b16 v[182:183], v143 offset:57344
	ds_read_b64_tr_b16 v[180:181], v140 offset:57344
	v_mfma_f32_16x16x32_bf16 v[76:79], v[212:215], v[12:15], v[72:75]
	v_mfma_f32_16x16x32_bf16 v[72:75], v[192:195], v[0:3], v[240:243]
	v_mfma_f32_16x16x32_bf16 v[72:75], v[200:203], v[4:7], v[72:75]
	s_waitcnt lgkmcnt(10)
	v_mfma_f32_16x16x32_bf16 v[60:63], v[220:223], v[68:71], v[60:63]
	ds_read_b64_tr_b16 v[152:153], v147 offset:49152
	ds_read_b64_tr_b16 v[154:155], v149 offset:49152
	ds_read_b64_tr_b16 v[178:179], v149 offset:57344
	ds_read_b64_tr_b16 v[176:177], v147 offset:57344
	ds_read_b64_tr_b16 v[184:185], v133 offset:49152
	v_mfma_f32_16x16x32_bf16 v[60:63], v[224:227], v[64:67], v[60:63]
	v_mfma_f32_16x16x32_bf16 v[56:59], v[228:231], v[68:71], v[56:59]
	s_waitcnt lgkmcnt(9)
	v_mfma_f32_16x16x32_bf16 v[56:59], v[88:91], v[64:67], v[56:59]
	ds_read_b64_tr_b16 v[186:187], v134 offset:49152
	ds_read_b64_tr_b16 v[190:191], v134 offset:57344
	ds_read_b64_tr_b16 v[188:189], v133 offset:57344
	ds_read_b64_tr_b16 v[196:197], v135 offset:49152
	ds_read_b64_tr_b16 v[198:199], v136 offset:49152
	ds_read_b64_tr_b16 v[206:207], v136 offset:57344
	v_mfma_f32_16x16x32_bf16 v[52:55], v[96:99], v[68:71], v[52:55]
	v_mfma_f32_16x16x32_bf16 v[52:55], v[92:95], v[64:67], v[52:55]
	s_waitcnt lgkmcnt(9)
	v_mfma_f32_16x16x32_bf16 v[48:51], v[172:175], v[68:71], v[48:51]
	ds_read_b64_tr_b16 v[204:205], v135 offset:57344
	ds_read_b64_tr_b16 v[212:213], v137 offset:49152
	ds_read_b64_tr_b16 v[214:215], v138 offset:49152
	ds_read_b64_tr_b16 v[194:195], v138 offset:57344
	ds_read_b64_tr_b16 v[192:193], v137 offset:57344
	v_mfma_f32_16x16x32_bf16 v[48:51], v[180:183], v[64:67], v[48:51]
	v_mfma_f32_16x16x32_bf16 v[32:35], v[152:155], v[68:71], v[32:35]
	s_waitcnt lgkmcnt(8)
	v_mfma_f32_16x16x32_bf16 v[32:35], v[176:179], v[64:67], v[32:35]
	v_mfma_f32_16x16x32_bf16 v[36:39], v[184:187], v[68:71], v[36:39]
	v_mfma_f32_16x16x32_bf16 v[36:39], v[188:191], v[64:67], v[36:39]
	s_waitcnt lgkmcnt(2)
	v_mfma_f32_16x16x32_bf16 v[40:43], v[196:199], v[68:71], v[40:43]
	v_mfma_f32_16x16x32_bf16 v[40:43], v[204:207], v[64:67], v[40:43]
	v_mfma_f32_16x16x32_bf16 v[72:75], v[208:211], v[8:11], v[72:75]
	v_mfma_f32_16x16x32_bf16 v[44:47], v[212:215], v[68:71], v[44:47]
	v_mfma_f32_16x16x32_bf16 v[72:75], v[216:219], v[12:15], v[72:75]
	s_waitcnt lgkmcnt(0)
	v_mfma_f32_16x16x32_bf16 v[44:47], v[192:195], v[64:67], v[44:47]
	s_cbranch_vccnz .LBB0_1960
	v_add_u32_e32 v64, 0, v109
	s_waitcnt vmcnt(3)
	ds_write_b128 v100, v[16:19] offset:16384
	s_waitcnt vmcnt(2)
	ds_write_b128 v124, v[20:23] offset:16384
	s_waitcnt vmcnt(1)
	ds_write_b128 v64, v[24:27] offset:32768
	v_add_u32_e32 v64, 0, v112
	s_waitcnt vmcnt(0)
	ds_write_b128 v64, v[28:31] offset:32768

.LBB0_1966:
	ds_read_b128 v[164:167], v129 offset:16384
	ds_read_b128 v[168:171], v130 offset:16384
	ds_read_b128 v[172:175], v131 offset:16384
	ds_read_b128 v[176:179], v129 offset:17408
	ds_read_b128 v[180:183], v132 offset:16384
	ds_read_b128 v[184:187], v130 offset:17408
	ds_read_b128 v[188:191], v131 offset:17408
	ds_read_b128 v[192:195], v129 offset:24576
	ds_read_b128 v[196:199], v132 offset:17408
	ds_read_b128 v[200:203], v130 offset:24576
	ds_read_b128 v[204:207], v131 offset:24576
	ds_read_b128 v[208:211], v129 offset:25600
	ds_read_b128 v[212:215], v132 offset:24576
	ds_read_b128 v[216:219], v130 offset:25600
	ds_read_b128 v[220:223], v131 offset:25600
	v_sub_f32_e32 v64, v84, v96
	v_exp_f32_e32 v96, v64
	v_sub_f32_e32 v64, v85, v97
	v_exp_f32_e32 v97, v64
	v_sub_f32_e32 v64, v86, v98
	v_exp_f32_e32 v98, v64
	v_sub_f32_e32 v64, v87, v99
	v_exp_f32_e32 v99, v64
	v_sub_f32_e32 v64, v80, v92
	v_exp_f32_e32 v152, v64
	v_sub_f32_e32 v64, v81, v93
	v_exp_f32_e32 v153, v64
	v_sub_f32_e32 v64, v82, v94
	v_exp_f32_e32 v154, v64
	v_sub_f32_e32 v64, v83, v95
	s_waitcnt lgkmcnt(10)
	v_mfma_f32_16x16x32_bf16 v[84:87], v[164:167], v[0:3], v[240:243]
	ds_read_b128 v[224:227], v132 offset:25600
	ds_read_b64_tr_b16 v[228:229], v146 offset:32768
	ds_read_b64_tr_b16 v[230:231], v148 offset:32768
	ds_read_b64_tr_b16 v[166:167], v148 offset:40960
	ds_read_b64_tr_b16 v[164:165], v146 offset:40960
	v_exp_f32_e32 v155, v64
	v_sub_f32_e32 v64, v76, v88
	v_mfma_f32_16x16x32_bf16 v[84:87], v[168:171], v[4:7], v[84:87]
	v_exp_f32_e32 v156, v64
	v_sub_f32_e32 v64, v77, v89
	v_mfma_f32_16x16x32_bf16 v[92:95], v[176:179], v[0:3], v[240:243]
	v_exp_f32_e32 v157, v64
	v_sub_f32_e32 v64, v78, v90
	v_exp_f32_e32 v158, v64
	v_sub_f32_e32 v64, v79, v91
	s_waitcnt lgkmcnt(10)
	v_mfma_f32_16x16x32_bf16 v[88:91], v[184:187], v[4:7], v[92:95]
	ds_read_b64_tr_b16 v[168:169], v139 offset:32768
	ds_read_b64_tr_b16 v[170:171], v142 offset:32768
	ds_read_b64_tr_b16 v[178:179], v142 offset:40960
	ds_read_b64_tr_b16 v[176:177], v139 offset:40960
	ds_read_b64_tr_b16 v[184:185], v141 offset:32768
	v_exp_f32_e32 v159, v64
	v_mfma_f32_16x16x32_bf16 v[80:83], v[172:175], v[8:11], v[84:87]
	v_sub_f32_e32 v64, v72, v66
	v_sub_f32_e32 v70, v73, v67
	v_mfma_f32_16x16x32_bf16 v[76:79], v[188:191], v[8:11], v[88:91]
	v_sub_f32_e32 v68, v74, v68
	s_and_b64 vcc, exec, s[6:7]
	v_mfma_f32_16x16x32_bf16 v[92:95], v[192:195], v[0:3], v[240:243]
	v_mfma_f32_16x16x32_bf16 v[76:79], v[196:199], v[12:15], v[76:79]
	v_mfma_f32_16x16x32_bf16 v[88:91], v[200:203], v[4:7], v[92:95]
	v_mfma_f32_16x16x32_bf16 v[80:83], v[180:183], v[12:15], v[80:83]
	v_exp_f32_e32 v160, v64
	v_exp_f32_e32 v161, v70
	s_waitcnt lgkmcnt(10)
	v_mfma_f32_16x16x32_bf16 v[84:87], v[204:207], v[8:11], v[88:91]
	ds_read_b64_tr_b16 v[186:187], v145 offset:32768
	ds_read_b64_tr_b16 v[174:175], v145 offset:40960
	ds_read_b64_tr_b16 v[172:173], v141 offset:40960
	ds_read_b64_tr_b16 v[188:189], v140 offset:32768
	ds_read_b64_tr_b16 v[190:191], v143 offset:32768
	v_exp_f32_e32 v162, v68
	v_mfma_f32_16x16x32_bf16 v[64:67], v[212:215], v[12:15], v[84:87]
	v_sub_f32_e32 v68, v75, v69
	v_exp_f32_e32 v163, v68
	v_mfma_f32_16x16x32_bf16 v[84:87], v[208:211], v[0:3], v[240:243]
	v_cvt_pk_bf16_f32 v92, v96, v97
	v_cvt_pk_bf16_f32 v93, v98, v99
	v_mfma_f32_16x16x32_bf16 v[84:87], v[216:219], v[4:7], v[84:87]
	v_cvt_pk_bf16_f32 v94, v152, v153
	v_cvt_pk_bf16_f32 v95, v154, v155
	v_mfma_f32_16x16x32_bf16 v[68:71], v[220:223], v[8:11], v[84:87]
	s_nop 4
	v_cvt_pk_bf16_f32 v84, v156, v157
	s_waitcnt lgkmcnt(10)
	v_mfma_f32_16x16x32_bf16 v[68:71], v[224:227], v[12:15], v[68:71]
	ds_read_b64_tr_b16 v[194:195], v143 offset:40960
	ds_read_b64_tr_b16 v[192:193], v140 offset:40960
	ds_read_b64_tr_b16 v[196:197], v147 offset:32768
	ds_read_b64_tr_b16 v[198:199], v149 offset:32768
	ds_read_b64_tr_b16 v[202:203], v149 offset:40960
	v_cvt_pk_bf16_f32 v85, v158, v159
	v_cvt_pk_bf16_f32 v86, v160, v161
	v_mfma_f32_16x16x32_bf16 v[60:63], v[228:231], v[92:95], v[60:63]
	v_cvt_pk_bf16_f32 v87, v162, v163
	s_nop 1
	v_mfma_f32_16x16x32_bf16 v[60:63], v[164:167], v[84:87], v[60:63]
	s_waitcnt lgkmcnt(9)
	v_mfma_f32_16x16x32_bf16 v[56:59], v[168:171], v[92:95], v[56:59]
	ds_read_b64_tr_b16 v[200:201], v147 offset:40960
	ds_read_b64_tr_b16 v[180:181], v133 offset:32768
	ds_read_b64_tr_b16 v[182:183], v134 offset:32768
	ds_read_b64_tr_b16 v[206:207], v134 offset:40960
	ds_read_b64_tr_b16 v[204:205], v133 offset:40960
	ds_read_b64_tr_b16 v[212:213], v135 offset:32768
	v_mfma_f32_16x16x32_bf16 v[56:59], v[176:179], v[84:87], v[56:59]
	v_mfma_f32_16x16x32_bf16 v[52:55], v[184:187], v[92:95], v[52:55]
	s_waitcnt lgkmcnt(9)
	v_mfma_f32_16x16x32_bf16 v[52:55], v[172:175], v[84:87], v[52:55]
	ds_read_b64_tr_b16 v[214:215], v136 offset:32768
	ds_read_b64_tr_b16 v[210:211], v136 offset:40960
	ds_read_b64_tr_b16 v[208:209], v135 offset:40960
	ds_read_b64_tr_b16 v[216:217], v137 offset:32768
	ds_read_b64_tr_b16 v[218:219], v138 offset:32768
	ds_read_b64_tr_b16 v[222:223], v138 offset:40960
	v_mfma_f32_16x16x32_bf16 v[48:51], v[188:191], v[92:95], v[48:51]
	v_mfma_f32_16x16x32_bf16 v[48:51], v[192:195], v[84:87], v[48:51]
	s_waitcnt lgkmcnt(9)
	v_mfma_f32_16x16x32_bf16 v[32:35], v[196:199], v[92:95], v[32:35]
	ds_read_b64_tr_b16 v[220:221], v137 offset:40960
	v_mfma_f32_16x16x32_bf16 v[32:35], v[200:203], v[84:87], v[32:35]
	v_mfma_f32_16x16x32_bf16 v[36:39], v[180:183], v[92:95], v[36:39]
	s_waitcnt lgkmcnt(4)
	v_mfma_f32_16x16x32_bf16 v[36:39], v[204:207], v[84:87], v[36:39]
	v_mfma_f32_16x16x32_bf16 v[40:43], v[212:215], v[92:95], v[40:43]
	v_mfma_f32_16x16x32_bf16 v[40:43], v[208:211], v[84:87], v[40:43]
	s_waitcnt lgkmcnt(0)
	v_mfma_f32_16x16x32_bf16 v[44:47], v[216:219], v[92:95], v[44:47]
	v_mfma_f32_16x16x32_bf16 v[44:47], v[220:223], v[84:87], v[44:47]
	s_cbranch_vccnz .LBB0_1968
	v_add_u32_e32 v72, 0, v109
	s_waitcnt vmcnt(3)
	ds_write_b128 v100, v[16:19]
	s_waitcnt vmcnt(2)
	ds_write_b128 v124, v[20:23]
	s_waitcnt vmcnt(1)
	ds_write_b128 v72, v[24:27] offset:49152
	v_add_u32_e32 v72, 0, v112
	s_waitcnt vmcnt(0)
	ds_write_b128 v72, v[28:31] offset:49152

.LBB0_2030:
	ds_read_b128 v[88:91], v128
	ds_read_b128 v[92:95], v128 offset:1024
	ds_read_b128 v[156:159], v129
	ds_read_b128 v[188:191], v129 offset:1024
	ds_read_b128 v[192:195], v130
	ds_read_b128 v[196:199], v130 offset:1024
	ds_read_b128 v[200:203], v131
	ds_read_b128 v[204:207], v131 offset:1024
	ds_read_b128 v[208:211], v128 offset:8192
	ds_read_b128 v[212:215], v128 offset:9216
	ds_read_b128 v[216:219], v129 offset:8192
	ds_read_b128 v[220:223], v129 offset:9216
	ds_read_b128 v[224:227], v130 offset:8192
	ds_read_b128 v[228:231], v130 offset:9216
	s_and_b64 vcc, exec, s[6:7]
	s_waitcnt lgkmcnt(9)
	v_mfma_f32_16x16x32_bf16 v[72:75], v[88:91], v[0:3], 0
	ds_read_b128 v[88:91], v131 offset:8192
	v_mfma_f32_16x16x32_bf16 v[80:83], v[92:95], v[0:3], 0
	ds_read_b128 v[92:95], v131 offset:9216
	v_mfma_f32_16x16x32_bf16 v[72:75], v[156:159], v[4:7], v[72:75]
	ds_read_b64_tr_b16 v[156:157], v140 offset:49152
	ds_read_b64_tr_b16 v[158:159], v141 offset:49152
	v_mfma_f32_16x16x32_bf16 v[72:75], v[192:195], v[8:11], v[72:75]
	ds_read_b64_tr_b16 v[194:195], v141 offset:57344
	ds_read_b64_tr_b16 v[192:193], v140 offset:57344
	s_waitcnt lgkmcnt(9)
	v_mfma_f32_16x16x32_bf16 v[76:79], v[200:203], v[12:15], v[72:75]
	ds_read_b64_tr_b16 v[200:201], v136 offset:49152
	ds_read_b64_tr_b16 v[202:203], v137 offset:49152
	v_mfma_f32_16x16x32_bf16 v[72:75], v[188:191], v[4:7], v[80:83]
	ds_read_b64_tr_b16 v[190:191], v137 offset:57344
	ds_read_b64_tr_b16 v[188:189], v136 offset:57344
	v_mfma_f32_16x16x32_bf16 v[72:75], v[196:199], v[8:11], v[72:75]
	ds_read_b64_tr_b16 v[196:197], v138 offset:49152
	ds_read_b64_tr_b16 v[198:199], v142 offset:49152
	v_mfma_f32_16x16x32_bf16 v[72:75], v[204:207], v[12:15], v[72:75]
	v_mfma_f32_16x16x32_bf16 v[80:83], v[208:211], v[0:3], 0
	v_mfma_f32_16x16x32_bf16 v[80:83], v[216:219], v[4:7], v[80:83]
	s_waitcnt lgkmcnt(9)
	v_mfma_f32_16x16x32_bf16 v[80:83], v[224:227], v[8:11], v[80:83]
	ds_read_b64_tr_b16 v[206:207], v142 offset:57344
	ds_read_b64_tr_b16 v[204:205], v138 offset:57344
	ds_read_b64_tr_b16 v[208:209], v139 offset:49152
	ds_read_b64_tr_b16 v[210:211], v143 offset:49152
	ds_read_b64_tr_b16 v[218:219], v143 offset:57344
	ds_read_b64_tr_b16 v[216:217], v139 offset:57344
	v_mfma_f32_16x16x32_bf16 v[84:87], v[88:91], v[12:15], v[80:83]
	v_mfma_f32_16x16x32_bf16 v[80:83], v[212:215], v[0:3], 0
	v_mfma_f32_16x16x32_bf16 v[80:83], v[220:223], v[4:7], v[80:83]
	s_waitcnt lgkmcnt(10)
	v_mfma_f32_16x16x32_bf16 v[48:51], v[156:159], v[68:71], v[48:51]
	ds_read_b64_tr_b16 v[224:225], v145 offset:49152
	ds_read_b64_tr_b16 v[226:227], v146 offset:49152
	ds_read_b64_tr_b16 v[90:91], v146 offset:57344
	ds_read_b64_tr_b16 v[88:89], v145 offset:57344
	ds_read_b64_tr_b16 v[212:213], v147 offset:49152
	v_mfma_f32_16x16x32_bf16 v[48:51], v[192:195], v[64:67], v[48:51]
	v_mfma_f32_16x16x32_bf16 v[40:43], v[200:203], v[68:71], v[40:43]
	s_waitcnt lgkmcnt(9)
	v_mfma_f32_16x16x32_bf16 v[40:43], v[188:191], v[64:67], v[40:43]
	ds_read_b64_tr_b16 v[214:215], v148 offset:49152
	ds_read_b64_tr_b16 v[222:223], v148 offset:57344
	ds_read_b64_tr_b16 v[220:221], v147 offset:57344
	ds_read_b64_tr_b16 v[156:157], v149 offset:49152
	ds_read_b64_tr_b16 v[158:159], v150 offset:49152
	ds_read_b64_tr_b16 v[194:195], v150 offset:57344
	v_mfma_f32_16x16x32_bf16 v[44:47], v[196:199], v[68:71], v[44:47]
	v_mfma_f32_16x16x32_bf16 v[44:47], v[204:207], v[64:67], v[44:47]
	s_waitcnt lgkmcnt(9)
	v_mfma_f32_16x16x32_bf16 v[56:59], v[208:211], v[68:71], v[56:59]
	ds_read_b64_tr_b16 v[192:193], v149 offset:57344
	ds_read_b64_tr_b16 v[200:201], v151 offset:49152
	ds_read_b64_tr_b16 v[202:203], v152 offset:49152
	ds_read_b64_tr_b16 v[190:191], v152 offset:57344
	ds_read_b64_tr_b16 v[188:189], v151 offset:57344
	v_mfma_f32_16x16x32_bf16 v[56:59], v[216:219], v[64:67], v[56:59]
	v_mfma_f32_16x16x32_bf16 v[60:63], v[224:227], v[68:71], v[60:63]
	s_waitcnt lgkmcnt(8)
	v_mfma_f32_16x16x32_bf16 v[60:63], v[88:91], v[64:67], v[60:63]
	v_mfma_f32_16x16x32_bf16 v[52:55], v[212:215], v[68:71], v[52:55]
	v_mfma_f32_16x16x32_bf16 v[52:55], v[220:223], v[64:67], v[52:55]
	s_waitcnt lgkmcnt(2)
	v_mfma_f32_16x16x32_bf16 v[32:35], v[156:159], v[68:71], v[32:35]
	v_mfma_f32_16x16x32_bf16 v[32:35], v[192:195], v[64:67], v[32:35]
	v_mfma_f32_16x16x32_bf16 v[80:83], v[228:231], v[8:11], v[80:83]
	v_mfma_f32_16x16x32_bf16 v[36:39], v[200:203], v[68:71], v[36:39]
	v_mfma_f32_16x16x32_bf16 v[80:83], v[92:95], v[12:15], v[80:83]
	s_waitcnt lgkmcnt(0)
	v_mfma_f32_16x16x32_bf16 v[36:39], v[188:191], v[64:67], v[36:39]
	s_cbranch_vccnz .LBB0_2032
	s_waitcnt vmcnt(3)
	ds_write_b128 v98, v[16:19] offset:16384
	s_waitcnt vmcnt(2)
	ds_write_b128 v99, v[20:23] offset:16384
	s_waitcnt vmcnt(1)
	ds_write_b128 v100, v[24:27] offset:32768
	s_waitcnt vmcnt(0)
	ds_write_b128 v124, v[28:31] offset:32768

.LBB0_2054:
	ds_read_b128 v[176:179], v128 offset:16384
	ds_read_b128 v[180:183], v128 offset:17408
	ds_read_b128 v[188:191], v129 offset:16384
	ds_read_b128 v[192:195], v130 offset:16384
	ds_read_b128 v[196:199], v131 offset:16384
	ds_read_b128 v[200:203], v129 offset:17408
	ds_read_b128 v[204:207], v130 offset:17408
	ds_read_b128 v[208:211], v129 offset:24576
	ds_read_b128 v[212:215], v131 offset:17408
	ds_read_b128 v[216:219], v128 offset:24576
	ds_read_b128 v[220:223], v130 offset:24576
	ds_read_b128 v[224:227], v128 offset:25600
	ds_read_b128 v[228:231], v131 offset:24576
	v_pk_mul_f32 v[184:185], v[66:67], v[68:69]
	s_waitcnt lgkmcnt(8)
	v_mfma_f32_16x16x32_bf16 v[160:163], v[176:179], v[0:3], 0
	ds_read_b128 v[176:179], v129 offset:25600
	v_mul_f32_e32 v70, v70, v71
	v_mul_f32_e32 v157, v70, v157
	v_mul_f32_e32 v159, v157, v159
	v_mfma_f32_16x16x32_bf16 v[164:167], v[180:183], v[0:3], 0
	ds_read_b128 v[180:183], v130 offset:25600
	v_mul_f32_e32 v186, v153, v159
	v_pk_mul_f32 v[64:65], v[64:65], v[96:97]
	v_pk_mul_f32 v[72:73], v[72:73], v[74:75]
	v_mfma_f32_16x16x32_bf16 v[160:163], v[188:191], v[4:7], v[160:163]
	ds_read_b128 v[188:191], v131 offset:25600
	v_pk_mul_f32 v[96:97], v[64:65], v[186:187] op_sel_hi:[1,0]
	v_pk_mul_f32 v[84:85], v[84:85], v[94:95]
	v_mfma_f32_16x16x32_bf16 v[66:69], v[192:195], v[8:11], v[160:163]
	ds_read_b64_tr_b16 v[192:193], v140 offset:32768
	ds_read_b64_tr_b16 v[194:195], v141 offset:32768
	v_cvt_pk_bf16_f32 v173, v96, v97
	v_pk_mul_f32 v[96:97], v[76:77], v[78:79]
	v_mfma_f32_16x16x32_bf16 v[68:71], v[196:199], v[12:15], v[66:69]
	ds_read_b64_tr_b16 v[198:199], v141 offset:40960
	ds_read_b64_tr_b16 v[196:197], v140 offset:40960
	v_pk_mul_f32 v[96:97], v[96:97], v[186:187] op_sel_hi:[1,0]
	v_pk_mul_f32 v[86:87], v[86:87], v[92:93]
	s_waitcnt lgkmcnt(10)
	v_mfma_f32_16x16x32_bf16 v[164:167], v[200:203], v[4:7], v[164:167]
	ds_read_b64_tr_b16 v[200:201], v136 offset:32768
	ds_read_b64_tr_b16 v[202:203], v137 offset:32768
	v_mul_f32_e64 v66, v184, v186
	v_mul_f32_e64 v67, v185, v186
	v_pk_mul_f32 v[80:81], v[80:81], v[82:83]
	v_cvt_pk_bf16_f32 v172, v66, v67
	v_mfma_f32_16x16x32_bf16 v[64:67], v[204:207], v[8:11], v[164:167]
	ds_read_b64_tr_b16 v[206:207], v137 offset:40960
	ds_read_b64_tr_b16 v[204:205], v136 offset:40960
	s_and_b64 vcc, exec, s[6:7]
	v_mfma_f32_16x16x32_bf16 v[64:67], v[212:215], v[12:15], v[64:67]
	ds_read_b64_tr_b16 v[212:213], v138 offset:32768
	v_mfma_f32_16x16x32_bf16 v[168:171], v[216:219], v[0:3], 0
	v_cvt_pk_bf16_f32 v174, v96, v97
	v_pk_mul_f32 v[96:97], v[72:73], v[186:187] op_sel_hi:[1,0]
	v_mfma_f32_16x16x32_bf16 v[76:79], v[208:211], v[4:7], v[168:171]
	v_cvt_pk_bf16_f32 v175, v96, v97
	s_waitcnt lgkmcnt(9)
	v_mfma_f32_16x16x32_bf16 v[94:97], v[224:227], v[0:3], 0
	ds_read_b64_tr_b16 v[214:215], v142 offset:32768
	ds_read_b64_tr_b16 v[218:219], v142 offset:40960
	ds_read_b64_tr_b16 v[216:217], v138 offset:40960
	ds_read_b64_tr_b16 v[208:209], v139 offset:32768
	ds_read_b64_tr_b16 v[210:211], v143 offset:32768
	ds_read_b64_tr_b16 v[226:227], v143 offset:40960
	v_mfma_f32_16x16x32_bf16 v[72:75], v[220:223], v[8:11], v[76:79]
	v_mul_f32_e32 v162, v153, v158
	v_pk_mul_f32 v[84:85], v[84:85], v[162:163] op_sel_hi:[1,0]
	v_pk_mul_f32 v[86:87], v[86:87], v[162:163] op_sel_hi:[1,0]
	v_mfma_f32_16x16x32_bf16 v[92:95], v[176:179], v[4:7], v[94:97]
	v_cvt_pk_bf16_f32 v84, v84, v85
	v_cvt_pk_bf16_f32 v85, v86, v87
	v_pk_mul_f32 v[86:87], v[88:89], v[90:91]
	v_mfma_f32_16x16x32_bf16 v[92:95], v[180:183], v[8:11], v[92:95]
	v_pk_mul_f32 v[86:87], v[86:87], v[162:163] op_sel_hi:[1,0]
	v_mfma_f32_16x16x32_bf16 v[76:79], v[188:191], v[12:15], v[92:95]
	v_cvt_pk_bf16_f32 v86, v86, v87
	s_nop 4
	v_pk_mul_f32 v[92:93], v[80:81], v[162:163] op_sel_hi:[1,0]
	s_waitcnt lgkmcnt(9)
	v_mfma_f32_16x16x32_bf16 v[48:51], v[192:195], v[172:175], v[48:51]
	ds_read_b64_tr_b16 v[224:225], v139 offset:40960
	ds_read_b64_tr_b16 v[220:221], v145 offset:32768
	ds_read_b64_tr_b16 v[222:223], v146 offset:32768
	ds_read_b64_tr_b16 v[178:179], v146 offset:40960
	ds_read_b64_tr_b16 v[176:177], v145 offset:40960
	ds_read_b64_tr_b16 v[180:181], v147 offset:32768
	v_cvt_pk_bf16_f32 v87, v92, v93
	v_mfma_f32_16x16x32_bf16 v[40:43], v[200:203], v[172:175], v[40:43]
	s_waitcnt lgkmcnt(9)
	v_mfma_f32_16x16x32_bf16 v[40:43], v[204:207], v[84:87], v[40:43]
	ds_read_b64_tr_b16 v[182:183], v148 offset:32768
	ds_read_b64_tr_b16 v[190:191], v148 offset:40960
	ds_read_b64_tr_b16 v[188:189], v147 offset:40960
	ds_read_b64_tr_b16 v[192:193], v149 offset:32768
	ds_read_b64_tr_b16 v[194:195], v150 offset:32768
	ds_read_b64_tr_b16 v[202:203], v150 offset:40960
	v_mfma_f32_16x16x32_bf16 v[44:47], v[212:215], v[172:175], v[44:47]
	v_mfma_f32_16x16x32_bf16 v[44:47], v[216:219], v[84:87], v[44:47]
	s_waitcnt lgkmcnt(9)
	v_mfma_f32_16x16x32_bf16 v[56:59], v[208:211], v[172:175], v[56:59]
	ds_read_b64_tr_b16 v[200:201], v149 offset:40960
	ds_read_b64_tr_b16 v[204:205], v151 offset:32768
	ds_read_b64_tr_b16 v[206:207], v152 offset:32768
	ds_read_b64_tr_b16 v[214:215], v152 offset:40960
	ds_read_b64_tr_b16 v[212:213], v151 offset:40960
	v_mfma_f32_16x16x32_bf16 v[56:59], v[224:227], v[84:87], v[56:59]
	v_mfma_f32_16x16x32_bf16 v[60:63], v[220:223], v[172:175], v[60:63]
	s_waitcnt lgkmcnt(8)
	v_mfma_f32_16x16x32_bf16 v[60:63], v[176:179], v[84:87], v[60:63]
	v_mfma_f32_16x16x32_bf16 v[52:55], v[180:183], v[172:175], v[52:55]
	v_mfma_f32_16x16x32_bf16 v[52:55], v[188:191], v[84:87], v[52:55]
	s_waitcnt lgkmcnt(2)
	v_mfma_f32_16x16x32_bf16 v[32:35], v[192:195], v[172:175], v[32:35]
	v_mfma_f32_16x16x32_bf16 v[32:35], v[200:203], v[84:87], v[32:35]
	v_mfma_f32_16x16x32_bf16 v[36:39], v[204:207], v[172:175], v[36:39]
	v_mfma_f32_16x16x32_bf16 v[72:75], v[228:231], v[12:15], v[72:75]
	v_mfma_f32_16x16x32_bf16 v[48:51], v[196:199], v[84:87], v[48:51]
	s_waitcnt lgkmcnt(0)
	v_mfma_f32_16x16x32_bf16 v[36:39], v[212:215], v[84:87], v[36:39]
	s_cbranch_vccnz .LBB0_2056
	s_waitcnt vmcnt(3)
	ds_write_b128 v98, v[16:19]
	s_waitcnt vmcnt(2)
	ds_write_b128 v99, v[20:23]
	s_waitcnt vmcnt(1)
	ds_write_b128 v100, v[24:27] offset:49152
	s_waitcnt vmcnt(0)
	ds_write_b128 v124, v[28:31] offset:49152

.LBB0_2133:
	ds_read_b128 v[88:91], v128
	ds_read_b128 v[92:95], v128 offset:1024
	ds_read_b128 v[156:159], v129
	ds_read_b128 v[188:191], v129 offset:1024
	ds_read_b128 v[192:195], v130
	ds_read_b128 v[196:199], v130 offset:1024
	ds_read_b128 v[200:203], v131
	ds_read_b128 v[204:207], v131 offset:1024
	ds_read_b128 v[208:211], v128 offset:8192
	ds_read_b128 v[212:215], v128 offset:9216
	ds_read_b128 v[216:219], v129 offset:8192
	ds_read_b128 v[220:223], v129 offset:9216
	ds_read_b128 v[224:227], v130 offset:8192
	ds_read_b128 v[228:231], v130 offset:9216
	s_and_b64 vcc, exec, s[6:7]
	s_waitcnt lgkmcnt(9)
	v_mfma_f32_16x16x32_bf16 v[72:75], v[88:91], v[0:3], 0
	ds_read_b128 v[88:91], v131 offset:8192
	v_mfma_f32_16x16x32_bf16 v[80:83], v[92:95], v[0:3], 0
	ds_read_b128 v[92:95], v131 offset:9216
	v_mfma_f32_16x16x32_bf16 v[72:75], v[156:159], v[4:7], v[72:75]
	ds_read_b64_tr_b16 v[156:157], v142 offset:49152
	ds_read_b64_tr_b16 v[158:159], v143 offset:49152
	v_mfma_f32_16x16x32_bf16 v[72:75], v[192:195], v[8:11], v[72:75]
	ds_read_b64_tr_b16 v[194:195], v143 offset:57344
	ds_read_b64_tr_b16 v[192:193], v142 offset:57344
	s_waitcnt lgkmcnt(9)
	v_mfma_f32_16x16x32_bf16 v[76:79], v[200:203], v[12:15], v[72:75]
	ds_read_b64_tr_b16 v[200:201], v136 offset:49152
	ds_read_b64_tr_b16 v[202:203], v139 offset:49152
	v_mfma_f32_16x16x32_bf16 v[72:75], v[188:191], v[4:7], v[80:83]
	ds_read_b64_tr_b16 v[190:191], v139 offset:57344
	ds_read_b64_tr_b16 v[188:189], v136 offset:57344
	v_mfma_f32_16x16x32_bf16 v[72:75], v[196:199], v[8:11], v[72:75]
	ds_read_b64_tr_b16 v[196:197], v138 offset:49152
	ds_read_b64_tr_b16 v[198:199], v141 offset:49152
	v_mfma_f32_16x16x32_bf16 v[72:75], v[204:207], v[12:15], v[72:75]
	v_mfma_f32_16x16x32_bf16 v[80:83], v[208:211], v[0:3], 0
	v_mfma_f32_16x16x32_bf16 v[80:83], v[216:219], v[4:7], v[80:83]
	s_waitcnt lgkmcnt(9)
	v_mfma_f32_16x16x32_bf16 v[80:83], v[224:227], v[8:11], v[80:83]
	ds_read_b64_tr_b16 v[206:207], v141 offset:57344
	ds_read_b64_tr_b16 v[204:205], v138 offset:57344
	ds_read_b64_tr_b16 v[208:209], v137 offset:49152
	ds_read_b64_tr_b16 v[210:211], v140 offset:49152
	ds_read_b64_tr_b16 v[218:219], v140 offset:57344
	ds_read_b64_tr_b16 v[216:217], v137 offset:57344
	v_mfma_f32_16x16x32_bf16 v[84:87], v[88:91], v[12:15], v[80:83]
	v_mfma_f32_16x16x32_bf16 v[80:83], v[212:215], v[0:3], 0
	v_mfma_f32_16x16x32_bf16 v[80:83], v[220:223], v[4:7], v[80:83]
	s_waitcnt lgkmcnt(10)
	v_mfma_f32_16x16x32_bf16 v[60:63], v[156:159], v[64:67], v[60:63]
	ds_read_b64_tr_b16 v[224:225], v145 offset:49152
	ds_read_b64_tr_b16 v[226:227], v146 offset:49152
	ds_read_b64_tr_b16 v[90:91], v146 offset:57344
	ds_read_b64_tr_b16 v[88:89], v145 offset:57344
	ds_read_b64_tr_b16 v[212:213], v147 offset:49152
	v_mfma_f32_16x16x32_bf16 v[60:63], v[192:195], v[68:71], v[60:63]
	v_mfma_f32_16x16x32_bf16 v[52:55], v[200:203], v[64:67], v[52:55]
	s_waitcnt lgkmcnt(9)
	v_mfma_f32_16x16x32_bf16 v[52:55], v[188:191], v[68:71], v[52:55]
	ds_read_b64_tr_b16 v[214:215], v148 offset:49152
	ds_read_b64_tr_b16 v[222:223], v148 offset:57344
	ds_read_b64_tr_b16 v[220:221], v147 offset:57344
	ds_read_b64_tr_b16 v[156:157], v149 offset:49152
	ds_read_b64_tr_b16 v[158:159], v150 offset:49152
	ds_read_b64_tr_b16 v[194:195], v150 offset:57344
	v_mfma_f32_16x16x32_bf16 v[44:47], v[196:199], v[64:67], v[44:47]
	v_mfma_f32_16x16x32_bf16 v[44:47], v[204:207], v[68:71], v[44:47]
	s_waitcnt lgkmcnt(9)
	v_mfma_f32_16x16x32_bf16 v[56:59], v[208:211], v[64:67], v[56:59]
	ds_read_b64_tr_b16 v[192:193], v149 offset:57344
	ds_read_b64_tr_b16 v[200:201], v151 offset:49152
	ds_read_b64_tr_b16 v[202:203], v152 offset:49152
	ds_read_b64_tr_b16 v[190:191], v152 offset:57344
	ds_read_b64_tr_b16 v[188:189], v151 offset:57344
	v_mfma_f32_16x16x32_bf16 v[56:59], v[216:219], v[68:71], v[56:59]
	v_mfma_f32_16x16x32_bf16 v[48:51], v[224:227], v[64:67], v[48:51]
	s_waitcnt lgkmcnt(8)
	v_mfma_f32_16x16x32_bf16 v[48:51], v[88:91], v[68:71], v[48:51]
	v_mfma_f32_16x16x32_bf16 v[40:43], v[212:215], v[64:67], v[40:43]
	v_mfma_f32_16x16x32_bf16 v[40:43], v[220:223], v[68:71], v[40:43]
	s_waitcnt lgkmcnt(2)
	v_mfma_f32_16x16x32_bf16 v[32:35], v[156:159], v[64:67], v[32:35]
	v_mfma_f32_16x16x32_bf16 v[32:35], v[192:195], v[68:71], v[32:35]
	v_mfma_f32_16x16x32_bf16 v[80:83], v[228:231], v[8:11], v[80:83]
	v_mfma_f32_16x16x32_bf16 v[36:39], v[200:203], v[64:67], v[36:39]
	v_mfma_f32_16x16x32_bf16 v[80:83], v[92:95], v[12:15], v[80:83]
	s_waitcnt lgkmcnt(0)
	v_mfma_f32_16x16x32_bf16 v[36:39], v[188:191], v[68:71], v[36:39]
	s_cbranch_vccnz .LBB0_2135
	s_waitcnt vmcnt(3)
	ds_write_b128 v98, v[16:19] offset:16384
	s_waitcnt vmcnt(2)
	ds_write_b128 v99, v[20:23] offset:16384
	s_waitcnt vmcnt(1)
	ds_write_b128 v100, v[24:27] offset:32768
	s_waitcnt vmcnt(0)
	ds_write_b128 v124, v[28:31] offset:32768

.LBB0_2157:
	ds_read_b128 v[176:179], v128 offset:16384
	ds_read_b128 v[180:183], v128 offset:17408
	ds_read_b128 v[188:191], v129 offset:16384
	ds_read_b128 v[192:195], v130 offset:16384
	ds_read_b128 v[196:199], v131 offset:16384
	ds_read_b128 v[200:203], v129 offset:17408
	ds_read_b128 v[204:207], v130 offset:17408
	ds_read_b128 v[208:211], v129 offset:24576
	ds_read_b128 v[212:215], v131 offset:17408
	ds_read_b128 v[216:219], v128 offset:24576
	ds_read_b128 v[220:223], v130 offset:24576
	ds_read_b128 v[224:227], v128 offset:25600
	ds_read_b128 v[228:231], v131 offset:24576
	v_pk_mul_f32 v[184:185], v[66:67], v[68:69]
	s_waitcnt lgkmcnt(8)
	v_mfma_f32_16x16x32_bf16 v[160:163], v[176:179], v[0:3], 0
	ds_read_b128 v[176:179], v129 offset:25600
	v_mul_f32_e32 v70, v70, v71
	v_mul_f32_e32 v157, v70, v157
	v_mul_f32_e32 v159, v157, v159
	v_mfma_f32_16x16x32_bf16 v[164:167], v[180:183], v[0:3], 0
	ds_read_b128 v[180:183], v130 offset:25600
	v_mul_f32_e32 v186, v153, v159
	v_pk_mul_f32 v[64:65], v[64:65], v[96:97]
	v_pk_mul_f32 v[72:73], v[72:73], v[74:75]
	v_mfma_f32_16x16x32_bf16 v[160:163], v[188:191], v[4:7], v[160:163]
	ds_read_b128 v[188:191], v131 offset:25600
	v_pk_mul_f32 v[96:97], v[64:65], v[186:187] op_sel_hi:[1,0]
	v_pk_mul_f32 v[84:85], v[84:85], v[94:95]
	v_mfma_f32_16x16x32_bf16 v[66:69], v[192:195], v[8:11], v[160:163]
	ds_read_b64_tr_b16 v[192:193], v142 offset:32768
	ds_read_b64_tr_b16 v[194:195], v143 offset:32768
	v_cvt_pk_bf16_f32 v173, v96, v97
	v_pk_mul_f32 v[96:97], v[76:77], v[78:79]
	v_mfma_f32_16x16x32_bf16 v[68:71], v[196:199], v[12:15], v[66:69]
	ds_read_b64_tr_b16 v[198:199], v143 offset:40960
	ds_read_b64_tr_b16 v[196:197], v142 offset:40960
	v_pk_mul_f32 v[96:97], v[96:97], v[186:187] op_sel_hi:[1,0]
	v_pk_mul_f32 v[86:87], v[86:87], v[92:93]
	s_waitcnt lgkmcnt(10)
	v_mfma_f32_16x16x32_bf16 v[164:167], v[200:203], v[4:7], v[164:167]
	ds_read_b64_tr_b16 v[200:201], v136 offset:32768
	ds_read_b64_tr_b16 v[202:203], v139 offset:32768
	v_mul_f32_e64 v66, v184, v186
	v_mul_f32_e64 v67, v185, v186
	v_pk_mul_f32 v[80:81], v[80:81], v[82:83]
	v_cvt_pk_bf16_f32 v172, v66, v67
	v_mfma_f32_16x16x32_bf16 v[64:67], v[204:207], v[8:11], v[164:167]
	ds_read_b64_tr_b16 v[206:207], v139 offset:40960
	ds_read_b64_tr_b16 v[204:205], v136 offset:40960
	s_and_b64 vcc, exec, s[6:7]
	v_mfma_f32_16x16x32_bf16 v[64:67], v[212:215], v[12:15], v[64:67]
	ds_read_b64_tr_b16 v[212:213], v138 offset:32768
	v_mfma_f32_16x16x32_bf16 v[168:171], v[216:219], v[0:3], 0
	v_cvt_pk_bf16_f32 v174, v96, v97
	v_pk_mul_f32 v[96:97], v[72:73], v[186:187] op_sel_hi:[1,0]
	v_mfma_f32_16x16x32_bf16 v[76:79], v[208:211], v[4:7], v[168:171]
	v_cvt_pk_bf16_f32 v175, v96, v97
	s_waitcnt lgkmcnt(9)
	v_mfma_f32_16x16x32_bf16 v[94:97], v[224:227], v[0:3], 0
	ds_read_b64_tr_b16 v[214:215], v141 offset:32768
	ds_read_b64_tr_b16 v[218:219], v141 offset:40960
	ds_read_b64_tr_b16 v[216:217], v138 offset:40960
	ds_read_b64_tr_b16 v[208:209], v137 offset:32768
	ds_read_b64_tr_b16 v[210:211], v140 offset:32768
	ds_read_b64_tr_b16 v[226:227], v140 offset:40960
	v_mfma_f32_16x16x32_bf16 v[72:75], v[220:223], v[8:11], v[76:79]
	v_mul_f32_e32 v162, v153, v158
	v_pk_mul_f32 v[84:85], v[84:85], v[162:163] op_sel_hi:[1,0]
	v_pk_mul_f32 v[86:87], v[86:87], v[162:163] op_sel_hi:[1,0]
	v_mfma_f32_16x16x32_bf16 v[92:95], v[176:179], v[4:7], v[94:97]
	v_cvt_pk_bf16_f32 v84, v84, v85
	v_cvt_pk_bf16_f32 v85, v86, v87
	v_pk_mul_f32 v[86:87], v[88:89], v[90:91]
	v_mfma_f32_16x16x32_bf16 v[92:95], v[180:183], v[8:11], v[92:95]
	v_pk_mul_f32 v[86:87], v[86:87], v[162:163] op_sel_hi:[1,0]
	v_mfma_f32_16x16x32_bf16 v[76:79], v[188:191], v[12:15], v[92:95]
	v_cvt_pk_bf16_f32 v86, v86, v87
	s_nop 4
	v_pk_mul_f32 v[92:93], v[80:81], v[162:163] op_sel_hi:[1,0]
	s_waitcnt lgkmcnt(9)
	v_mfma_f32_16x16x32_bf16 v[60:63], v[192:195], v[172:175], v[60:63]
	ds_read_b64_tr_b16 v[224:225], v137 offset:40960
	ds_read_b64_tr_b16 v[220:221], v145 offset:32768
	ds_read_b64_tr_b16 v[222:223], v146 offset:32768
	ds_read_b64_tr_b16 v[178:179], v146 offset:40960
	ds_read_b64_tr_b16 v[176:177], v145 offset:40960
	ds_read_b64_tr_b16 v[180:181], v147 offset:32768
	v_cvt_pk_bf16_f32 v87, v92, v93
	v_mfma_f32_16x16x32_bf16 v[52:55], v[200:203], v[172:175], v[52:55]
	s_waitcnt lgkmcnt(9)
	v_mfma_f32_16x16x32_bf16 v[52:55], v[204:207], v[84:87], v[52:55]
	ds_read_b64_tr_b16 v[182:183], v148 offset:32768
	ds_read_b64_tr_b16 v[190:191], v148 offset:40960
	ds_read_b64_tr_b16 v[188:189], v147 offset:40960
	ds_read_b64_tr_b16 v[192:193], v149 offset:32768
	ds_read_b64_tr_b16 v[194:195], v150 offset:32768
	ds_read_b64_tr_b16 v[202:203], v150 offset:40960
	v_mfma_f32_16x16x32_bf16 v[44:47], v[212:215], v[172:175], v[44:47]
	v_mfma_f32_16x16x32_bf16 v[44:47], v[216:219], v[84:87], v[44:47]
	s_waitcnt lgkmcnt(9)
	v_mfma_f32_16x16x32_bf16 v[56:59], v[208:211], v[172:175], v[56:59]
	ds_read_b64_tr_b16 v[200:201], v149 offset:40960
	ds_read_b64_tr_b16 v[204:205], v151 offset:32768
	ds_read_b64_tr_b16 v[206:207], v152 offset:32768
	ds_read_b64_tr_b16 v[214:215], v152 offset:40960
	ds_read_b64_tr_b16 v[212:213], v151 offset:40960
	v_mfma_f32_16x16x32_bf16 v[56:59], v[224:227], v[84:87], v[56:59]
	v_mfma_f32_16x16x32_bf16 v[48:51], v[220:223], v[172:175], v[48:51]
	s_waitcnt lgkmcnt(8)
	v_mfma_f32_16x16x32_bf16 v[48:51], v[176:179], v[84:87], v[48:51]
	v_mfma_f32_16x16x32_bf16 v[40:43], v[180:183], v[172:175], v[40:43]
	v_mfma_f32_16x16x32_bf16 v[40:43], v[188:191], v[84:87], v[40:43]
	s_waitcnt lgkmcnt(2)
	v_mfma_f32_16x16x32_bf16 v[32:35], v[192:195], v[172:175], v[32:35]
	v_mfma_f32_16x16x32_bf16 v[32:35], v[200:203], v[84:87], v[32:35]
	v_mfma_f32_16x16x32_bf16 v[36:39], v[204:207], v[172:175], v[36:39]
	v_mfma_f32_16x16x32_bf16 v[72:75], v[228:231], v[12:15], v[72:75]
	v_mfma_f32_16x16x32_bf16 v[60:63], v[196:199], v[84:87], v[60:63]
	s_waitcnt lgkmcnt(0)
	v_mfma_f32_16x16x32_bf16 v[36:39], v[212:215], v[84:87], v[36:39]
	s_cbranch_vccnz .LBB0_2159
	s_waitcnt vmcnt(3)
	ds_write_b128 v98, v[16:19]
	s_waitcnt vmcnt(2)
	ds_write_b128 v99, v[20:23]
	s_waitcnt vmcnt(1)
	ds_write_b128 v100, v[24:27] offset:49152
	s_waitcnt vmcnt(0)
	ds_write_b128 v124, v[28:31] offset:49152
